# prep32 stage B4: final cross-row step of the two per-token wave reductions uses v_permlane16_swap instead of an LDS bpermute round trip
# speedup vs baseline: 1.0049x; 1.0049x over previous
.LBB0_405:
	s_lshl_b32 s20, s0, 4
	s_mul_i32 s1, s0, 0x3000
	s_or_b32 s21, s20, 1
	v_add_u32_e32 v89, s1, v57
	s_mul_i32 s1, s21, 0x300
	v_add_u32_e32 v86, s1, v57
	s_add_i32 s1, s1, 0
	s_add_i32 s22, s1, 0x1b800
	s_waitcnt lgkmcnt(0)
	v_lshlrev_b32_e32 v60, 1, v46
	v_add_u32_e32 v91, s22, v60
	s_add_i32 s22, s1, 0x1bb00
	v_add_u32_e32 v94, s22, v60
	s_add_i32 s22, s1, 0x1be00
	v_add_u32_e32 v95, s22, v60
	s_add_i32 s22, s1, 0x1c100
	v_add_u32_e32 v59, s22, v60
	s_add_i32 s22, s1, 0x1c400
	v_add_u32_e32 v61, s22, v60
	s_add_i32 s22, s1, 0x1c700
	v_add_u32_e32 v62, s22, v60
	s_add_i32 s22, s1, 0x1ca00
	v_add_u32_e32 v63, s22, v60
	s_add_i32 s22, s1, 0x1cd00
	ds_read_u16 v83, v95 offset:24576
	ds_read_u16 v81, v59 offset:24576
	ds_read_u16 v79, v61 offset:24576
	ds_read_u16 v77, v62 offset:24576
	ds_read_u16 v73, v63 offset:768
	ds_read_u16 v75, v62 offset:768
	ds_read_u16 v78, v61 offset:768
	ds_read_u16 v80, v59 offset:768
	ds_read_u16 v76, v63 offset:24576
	v_add_u32_e32 v59, s22, v60
	s_add_i32 s22, s1, 0x1d000
	ds_read_u16 v74, v59 offset:24576
	ds_read_u16 v71, v59 offset:768
	v_add_u32_e32 v59, s22, v60
	s_add_i32 s22, s1, 0x1d300
	ds_read_u16 v72, v59 offset:24576
	ds_read_u16 v69, v59 offset:768
	v_add_u32_e32 v59, s22, v60
	s_add_i32 s22, s1, 0x1d600
	ds_read_u16 v70, v59 offset:24576
	ds_read_u16 v67, v59 offset:768
	v_add_u32_e32 v59, s22, v60
	s_add_i32 s22, s1, 0x1d900
	ds_read_u16 v68, v59 offset:24576
	ds_read_u16 v65, v59 offset:768
	v_add_u32_e32 v59, s22, v60
	s_add_i32 s22, s1, 0x1dc00
	ds_read_u16 v66, v59 offset:24576
	ds_read_u16 v63, v59 offset:768
	v_add_u32_e32 v59, s22, v60
	s_add_i32 s22, s1, 0x1df00
	s_add_i32 s1, s1, 0x1e200
	s_mul_i32 s0, s0, 0xb000
	ds_read_u16 v64, v59 offset:24576
	ds_read_u16 v61, v59 offset:768
	v_add_u32_e32 v59, s22, v60
	v_add_u32_e32 v60, s1, v60
	v_add_u32_e32 v87, s0, v58
	ds_read_u16 v62, v59 offset:24576
	ds_read_u16 v59, v59 offset:768
	ds_read_u16 v60, v60 offset:24576
	ds_read_u16 v82, v87 offset:3584
	ds_read_u16 v84, v87 offset:768
	ds_read_u16 v85, v87 offset:6400
	ds_read_u16 v96, v87 offset:4352
	ds_read_u16 v98, v87 offset:5632
	ds_read_u16 v97, v87 offset:2816
	s_waitcnt lgkmcnt(5)
	v_lshlrev_b32_e32 v82, 16, v82
	s_waitcnt lgkmcnt(3)
	v_lshlrev_b32_e32 v85, 16, v85
	v_lshlrev_b32_e32 v84, 16, v84
	v_pk_add_f32 v[84:85], v[84:85], v[82:83] op_sel_hi:[1,0] neg_lo:[0,1] neg_hi:[0,1]
	ds_read_u16 v88, v87 offset:1536
	ds_read_u16 v92, v87
	v_pk_mul_f32 v[84:85], v[54:55], v[84:85]
	ds_read_u16 v99, v87 offset:7168
	v_add_f32_e32 v82, v84, v82
	v_add_f32_e32 v90, v82, v85
	v_mul_f32_e32 v100, v0, v90
	v_mul_f32_e32 v82, v100, v100
	v_mov_b32_e32 v84, v1
	s_waitcnt lgkmcnt(2)
	v_lshlrev_b32_e32 v93, 16, v88
	s_waitcnt lgkmcnt(1)
	v_lshlrev_b32_e32 v92, 16, v92
	v_mov_b32_dpp v84, v82 quad_perm:[1,0,3,2] row_mask:0xf bank_mask:0xf
	v_fmac_f32_e32 v84, v100, v100
	s_or_b32 s22, s20, s76
	s_nop 0
	v_add_f32_dpp v82, v84, v84 quad_perm:[2,3,0,1] row_mask:0xf bank_mask:0xf bound_ctrl:1
	s_nop 1
	v_add_f32_dpp v82, v82, v82 row_half_mirror row_mask:0xf bank_mask:0xf bound_ctrl:1
	s_nop 1
	v_add_f32_dpp v101, v82, v82 row_mirror row_mask:0xf bank_mask:0xf bound_ctrl:1
	ds_read_u16 v87, v86
	ds_read_u16 v88, v91 offset:24576
	ds_read_u16 v85, v94 offset:24576
	ds_read_u16 v82, v95 offset:768
	ds_read_u16 v84, v94 offset:768
	ds_read_u16 v86, v91 offset:768
	ds_read_u16 v91, v89
	ds_read_u16 v89, v89 offset:24576
	v_mov_b32_e32 v94, v101
	s_nop 1
	v_permlane32_swap_b32 v101, v94
	v_lshlrev_b32_e32 v95, 16, v96
	v_add_f32_e32 v101, v101, v94
	v_mov_b32_e32 v102, v101
	s_nop 1
	v_permlane16_swap_b32_e32 v101, v102
	v_lshlrev_b32_e32 v96, 16, v98
	v_lshlrev_b32_e32 v94, 16, v97
	s_waitcnt lgkmcnt(8)
	v_lshlrev_b32_e32 v97, 16, v99
	v_pk_add_f32 v[92:93], v[92:93], v[94:95] neg_lo:[0,1] neg_hi:[0,1]
	s_waitcnt lgkmcnt(0)
	v_add_f32_e32 v98, v101, v102
	v_mul_f32_e32 v99, 0x4f800000, v98
	v_cmp_gt_f32_e32 vcc, s45, v98
	v_pk_fma_f32 v[92:93], v[50:51], v[92:93], v[94:95]
	v_pk_add_f32 v[94:95], v[96:97], v[94:95] neg_lo:[0,1] neg_hi:[0,1]
	v_cndmask_b32_e32 v98, v98, v99, vcc
	v_sqrt_f32_e32 v99, v98
	v_pk_fma_f32 v[92:93], v[52:53], v[94:95], v[92:93]
	v_add_u32_e32 v96, -1, v99
	v_fma_f32 v97, -v96, v99, v98
	v_cmp_ge_f32_e64 s[0:1], 0, v97
	v_add_u32_e32 v97, 1, v99
	s_nop 0
	v_cndmask_b32_e64 v96, v99, v96, s[0:1]
	v_fma_f32 v99, -v97, v99, v98
	v_cmp_lt_f32_e64 s[0:1], 0, v99
	s_nop 1
	v_cndmask_b32_e64 v96, v96, v97, s[0:1]
	v_mul_f32_e32 v97, 0x37800000, v96
	v_cndmask_b32_e32 v96, v96, v97, vcc
	v_cmp_class_f32_e32 vcc, v98, v207
	s_nop 1
	v_cndmask_b32_e32 v96, v96, v98, vcc
	v_max_f32_e32 v98, 0x2b8cbccc, v96
	v_div_scale_f32 v99, s[0:1], v98, v98, v100
	v_rcp_f32_e32 v101, v99
	v_mad_i64_i32 v[96:97], s[0:1], s22, v214, v[46:47]
	v_fma_f32 v94, -v99, v101, 1.0
	v_fmac_f32_e32 v101, v94, v101
	v_div_scale_f32 v94, vcc, v100, v98, v100
	v_mul_f32_e32 v95, v94, v101
	v_fma_f32 v102, -v99, v95, v94
	v_fmac_f32_e32 v95, v102, v101
	v_fma_f32 v94, -v99, v95, v94
	v_div_fmas_f32 v94, v94, v101, v95
	v_div_fixup_f32 v94, v94, v98, v100
	v_lshlrev_b32_e32 v99, 16, v89
	v_lshlrev_b32_e32 v98, 16, v91
	v_pk_add_f32 v[100:101], v[98:99], -1.0 op_sel_hi:[1,0]
	s_nop 0
	v_pk_fma_f32 v[100:101], v[48:49], v[100:101], 1.0 op_sel_hi:[1,1,0]
	s_nop 0
	v_pk_mul_f32 v[100:101], v[100:101], v[90:91] op_sel_hi:[1,0]
	v_mov_b32_e32 v91, v1
	v_add_f32_e32 v89, v100, v101
	v_mul_f32_e32 v89, v92, v89
	v_mul_f32_e32 v90, v56, v89
	v_cvt_pk_bf16_f32 v92, v92, v93
	v_cvt_pk_bf16_f32 v93, v94, 0
	v_mov_b32_dpp v91, v90 quad_perm:[1,0,3,2] row_mask:0xf bank_mask:0xf
	v_fmac_f32_e32 v91, v56, v89
	v_pk_mul_f32 v[94:95], v[94:95], v[98:99] op_sel_hi:[0,1]
	v_cvt_pk_bf16_f32 v94, v94, v95
	v_add_f32_dpp v89, v91, v91 quad_perm:[2,3,0,1] row_mask:0xf bank_mask:0xf bound_ctrl:1
	v_cvt_pk_bf16_f32 v95, v100, v101
	v_lshl_add_u64 v[98:99], v[96:97], 4, s[52:53]
	v_add_f32_dpp v89, v89, v89 row_half_mirror row_mask:0xf bank_mask:0xf bound_ctrl:1
	s_nop 1
	v_add_f32_dpp v89, v89, v89 row_mirror row_mask:0xf bank_mask:0xf bound_ctrl:1
	v_mov_b32_e32 v90, v89
	s_nop 1
	v_permlane32_swap_b32 v89, v90
	global_store_dwordx4 v[98:99], v[92:95], off
	v_add_f32_e32 v89, v89, v90
	v_mov_b32_e32 v90, v89
	s_nop 1
	v_permlane16_swap_b32_e32 v89, v90
	v_lshl_add_u64 v[94:95], v[96:97], 1, s[58:59]
	global_store_short_d16_hi v[94:95], v92, off
	s_and_saveexec_b64 s[0:1], s[42:43]
	s_cbranch_execz .LBB0_407
	s_waitcnt lgkmcnt(0)
	v_add_f32_e32 v89, v89, v90
	v_mad_i64_i32 v[90:91], s[22:23], s22, 24, v[114:115]
	global_store_dword v[90:91], v89, off
.LBB0_407:
	s_or_b64 exec, exec, s[0:1]
	s_or_b32 s22, s21, s76
	s_mulk_i32 s21, 0xb00
	v_lshlrev_b32_e32 v92, 16, v87
	v_add_u32_e32 v87, s21, v58
	v_lshlrev_b32_e32 v93, 16, v88
	ds_read_u16 v88, v87 offset:3584
	ds_read_u16 v89, v87 offset:768
	s_waitcnt lgkmcnt(2)
	ds_read_u16 v90, v87 offset:6400
	ds_read_u16 v94, v87 offset:4352
	ds_read_u16 v96, v87 offset:5632
	ds_read_u16 v97, v87 offset:2816
	s_waitcnt lgkmcnt(5)
	v_lshlrev_b32_e32 v88, 16, v88
	s_waitcnt lgkmcnt(3)
	v_lshlrev_b32_e32 v91, 16, v90
	v_lshlrev_b32_e32 v90, 16, v89
	ds_read_u16 v95, v87 offset:1536
	ds_read_u16 v98, v87
	v_pk_add_f32 v[90:91], v[90:91], v[88:89] op_sel_hi:[1,0] neg_lo:[0,1] neg_hi:[0,1]
	ds_read_u16 v87, v87 offset:7168
	v_pk_mul_f32 v[90:91], v[54:55], v[90:91]
	s_waitcnt lgkmcnt(4)
	v_lshlrev_b32_e32 v96, 16, v96
	v_add_f32_e32 v88, v90, v88
	v_add_f32_e32 v88, v88, v91
	v_mul_f32_e32 v89, v0, v88
	s_waitcnt lgkmcnt(2)
	v_lshlrev_b32_e32 v91, 16, v95
	s_waitcnt lgkmcnt(1)
	v_lshlrev_b32_e32 v90, 16, v98
	v_mul_f32_e32 v95, v89, v89
	v_mov_b32_e32 v98, v1
	s_nop 1
	v_mov_b32_dpp v98, v95 quad_perm:[1,0,3,2] row_mask:0xf bank_mask:0xf
	v_fmac_f32_e32 v98, v89, v89
	s_nop 1
	v_add_f32_dpp v95, v98, v98 quad_perm:[2,3,0,1] row_mask:0xf bank_mask:0xf bound_ctrl:1
	s_nop 1
	v_add_f32_dpp v95, v95, v95 row_half_mirror row_mask:0xf bank_mask:0xf bound_ctrl:1
	s_nop 1
	v_add_f32_dpp v95, v95, v95 row_mirror row_mask:0xf bank_mask:0xf bound_ctrl:1
	v_mov_b32_e32 v98, v95
	s_nop 1
	v_permlane32_swap_b32 v95, v98
	s_nop 0
	v_add_f32_e32 v98, v95, v98
	v_mov_b32_e32 v99, v98
	s_nop 1
	v_permlane16_swap_b32_e32 v98, v99
	v_lshlrev_b32_e32 v95, 16, v94
	v_lshlrev_b32_e32 v94, 16, v97
	s_waitcnt lgkmcnt(0)
	v_lshlrev_b32_e32 v97, 16, v87
	v_pk_add_f32 v[90:91], v[90:91], v[94:95] neg_lo:[0,1] neg_hi:[0,1]
	s_waitcnt lgkmcnt(0)
	v_add_f32_e32 v87, v98, v99
	v_mul_f32_e32 v98, 0x4f800000, v87
	v_cmp_gt_f32_e32 vcc, s45, v87
	v_pk_fma_f32 v[90:91], v[50:51], v[90:91], v[94:95]
	v_pk_add_f32 v[94:95], v[96:97], v[94:95] neg_lo:[0,1] neg_hi:[0,1]
	v_cndmask_b32_e32 v87, v87, v98, vcc
	v_sqrt_f32_e32 v98, v87
	v_pk_fma_f32 v[90:91], v[52:53], v[94:95], v[90:91]
	v_add_u32_e32 v96, -1, v98
	v_fma_f32 v97, -v96, v98, v87
	v_cmp_ge_f32_e64 s[0:1], 0, v97
	v_add_u32_e32 v97, 1, v98
	s_nop 0
	v_cndmask_b32_e64 v96, v98, v96, s[0:1]
	v_fma_f32 v98, -v97, v98, v87
	v_cmp_lt_f32_e64 s[0:1], 0, v98
	s_nop 1
	v_cndmask_b32_e64 v96, v96, v97, s[0:1]
	v_mul_f32_e32 v97, 0x37800000, v96
	v_cndmask_b32_e32 v96, v96, v97, vcc
	v_cmp_class_f32_e32 vcc, v87, v207
	v_mad_i64_i32 v[94:95], s[0:1], s22, v214, v[46:47]
	s_nop 0
	v_cndmask_b32_e32 v87, v96, v87, vcc
	v_max_f32_e32 v87, 0x2b8cbccc, v87
	v_div_scale_f32 v96, s[0:1], v87, v87, v89
	v_rcp_f32_e32 v97, v96
	s_nop 0
	v_fma_f32 v98, -v96, v97, 1.0
	v_fmac_f32_e32 v97, v98, v97
	v_div_scale_f32 v98, vcc, v89, v87, v89
	v_mul_f32_e32 v99, v98, v97
	v_fma_f32 v100, -v96, v99, v98
	v_fmac_f32_e32 v99, v100, v97
	v_fma_f32 v96, -v96, v99, v98
	v_div_fmas_f32 v96, v96, v97, v99
	v_pk_add_f32 v[98:99], v[92:93], -1.0 op_sel_hi:[1,0]
	v_div_fixup_f32 v96, v96, v87, v89
	v_pk_fma_f32 v[98:99], v[48:49], v[98:99], 1.0 op_sel_hi:[1,1,0]
	v_pk_mul_f32 v[92:93], v[96:97], v[92:93] op_sel_hi:[0,1]
	v_pk_mul_f32 v[98:99], v[98:99], v[88:89] op_sel_hi:[1,0]
	v_mov_b32_e32 v89, v1
	v_add_f32_e32 v87, v98, v99
	v_mul_f32_e32 v87, v90, v87
	v_mul_f32_e32 v88, v56, v87
	v_cvt_pk_bf16_f32 v90, v90, v91
	v_cvt_pk_bf16_f32 v91, v96, 0
	v_mov_b32_dpp v89, v88 quad_perm:[1,0,3,2] row_mask:0xf bank_mask:0xf
	v_fmac_f32_e32 v89, v56, v87
	v_cvt_pk_bf16_f32 v92, v92, v93
	v_cvt_pk_bf16_f32 v93, v98, v99
	v_add_f32_dpp v87, v89, v89 quad_perm:[2,3,0,1] row_mask:0xf bank_mask:0xf bound_ctrl:1
	v_lshl_add_u64 v[96:97], v[94:95], 4, s[52:53]
	s_nop 0
	v_add_f32_dpp v87, v87, v87 row_half_mirror row_mask:0xf bank_mask:0xf bound_ctrl:1
	s_nop 1
	v_add_f32_dpp v87, v87, v87 row_mirror row_mask:0xf bank_mask:0xf bound_ctrl:1
	v_mov_b32_e32 v88, v87
	s_nop 1
	v_permlane32_swap_b32 v87, v88
	global_store_dwordx4 v[96:97], v[90:93], off
	v_add_f32_e32 v87, v87, v88
	v_mov_b32_e32 v88, v87
	s_nop 1
	v_permlane16_swap_b32_e32 v87, v88
	v_lshl_add_u64 v[92:93], v[94:95], 1, s[58:59]
	global_store_short_d16_hi v[92:93], v90, off
	s_and_saveexec_b64 s[0:1], s[42:43]
	s_cbranch_execz .LBB0_409
	s_waitcnt lgkmcnt(0)
	v_add_f32_e32 v87, v87, v88
	v_mad_i64_i32 v[88:89], s[22:23], s22, 24, v[114:115]
	global_store_dword v[88:89], v87, off
.LBB0_409:
	s_or_b64 exec, exec, s[0:1]
	s_addk_i32 s21, 0xb00
	v_lshlrev_b32_e32 v91, 16, v85
	v_add_u32_e32 v85, s21, v58
	v_lshlrev_b32_e32 v90, 16, v86
	ds_read_u16 v86, v85 offset:3584
	ds_read_u16 v87, v85 offset:768
	s_waitcnt lgkmcnt(2)
	ds_read_u16 v88, v85 offset:6400
	ds_read_u16 v92, v85 offset:4352
	ds_read_u16 v94, v85 offset:5632
	ds_read_u16 v95, v85 offset:2816
	s_waitcnt lgkmcnt(5)
	v_lshlrev_b32_e32 v86, 16, v86
	s_waitcnt lgkmcnt(3)
	v_lshlrev_b32_e32 v89, 16, v88
	v_lshlrev_b32_e32 v88, 16, v87
	ds_read_u16 v93, v85 offset:1536
	ds_read_u16 v96, v85
	v_pk_add_f32 v[88:89], v[88:89], v[86:87] op_sel_hi:[1,0] neg_lo:[0,1] neg_hi:[0,1]
	ds_read_u16 v85, v85 offset:7168
	v_pk_mul_f32 v[88:89], v[54:55], v[88:89]
	s_waitcnt lgkmcnt(4)
	v_lshlrev_b32_e32 v94, 16, v94
	v_add_f32_e32 v86, v88, v86
	v_add_f32_e32 v86, v86, v89
	v_mul_f32_e32 v87, v0, v86
	s_waitcnt lgkmcnt(2)
	v_lshlrev_b32_e32 v89, 16, v93
	s_waitcnt lgkmcnt(1)
	v_lshlrev_b32_e32 v88, 16, v96
	v_mul_f32_e32 v93, v87, v87
	v_mov_b32_e32 v96, v1
	s_or_b32 s22, s20, s6
	s_nop 0
	v_mov_b32_dpp v96, v93 quad_perm:[1,0,3,2] row_mask:0xf bank_mask:0xf
	v_fmac_f32_e32 v96, v87, v87
	s_nop 1
	v_add_f32_dpp v93, v96, v96 quad_perm:[2,3,0,1] row_mask:0xf bank_mask:0xf bound_ctrl:1
	s_nop 1
	v_add_f32_dpp v93, v93, v93 row_half_mirror row_mask:0xf bank_mask:0xf bound_ctrl:1
	s_nop 1
	v_add_f32_dpp v93, v93, v93 row_mirror row_mask:0xf bank_mask:0xf bound_ctrl:1
	v_mov_b32_e32 v96, v93
	s_nop 1
	v_permlane32_swap_b32 v93, v96
	s_nop 0
	v_add_f32_e32 v96, v93, v96
	v_mov_b32_e32 v97, v96
	s_nop 1
	v_permlane16_swap_b32_e32 v96, v97
	v_lshlrev_b32_e32 v93, 16, v92
	v_lshlrev_b32_e32 v92, 16, v95
	s_waitcnt lgkmcnt(0)
	v_lshlrev_b32_e32 v95, 16, v85
	v_pk_add_f32 v[88:89], v[88:89], v[92:93] neg_lo:[0,1] neg_hi:[0,1]
	s_waitcnt lgkmcnt(0)
	v_add_f32_e32 v85, v96, v97
	v_mul_f32_e32 v96, 0x4f800000, v85
	v_cmp_gt_f32_e32 vcc, s45, v85
	v_pk_fma_f32 v[88:89], v[50:51], v[88:89], v[92:93]
	v_pk_add_f32 v[92:93], v[94:95], v[92:93] neg_lo:[0,1] neg_hi:[0,1]
	v_cndmask_b32_e32 v85, v85, v96, vcc
	v_sqrt_f32_e32 v96, v85
	v_pk_fma_f32 v[88:89], v[52:53], v[92:93], v[88:89]
	v_add_u32_e32 v94, -1, v96
	v_fma_f32 v95, -v94, v96, v85
	v_cmp_ge_f32_e64 s[0:1], 0, v95
	v_add_u32_e32 v95, 1, v96
	s_nop 0
	v_cndmask_b32_e64 v94, v96, v94, s[0:1]
	v_fma_f32 v96, -v95, v96, v85
	v_cmp_lt_f32_e64 s[0:1], 0, v96
	s_nop 1
	v_cndmask_b32_e64 v94, v94, v95, s[0:1]
	v_mul_f32_e32 v95, 0x37800000, v94
	v_cndmask_b32_e32 v94, v94, v95, vcc
	v_cmp_class_f32_e32 vcc, v85, v207
	v_mad_i64_i32 v[92:93], s[0:1], s22, v214, v[46:47]
	s_nop 0
	v_cndmask_b32_e32 v85, v94, v85, vcc
	v_max_f32_e32 v85, 0x2b8cbccc, v85
	v_div_scale_f32 v94, s[0:1], v85, v85, v87
	v_rcp_f32_e32 v95, v94
	s_nop 0
	v_fma_f32 v96, -v94, v95, 1.0
	v_fmac_f32_e32 v95, v96, v95
	v_div_scale_f32 v96, vcc, v87, v85, v87
	v_mul_f32_e32 v97, v96, v95
	v_fma_f32 v98, -v94, v97, v96
	v_fmac_f32_e32 v97, v98, v95
	v_fma_f32 v94, -v94, v97, v96
	v_div_fmas_f32 v94, v94, v95, v97
	v_pk_add_f32 v[96:97], v[90:91], -1.0 op_sel_hi:[1,0]
	v_div_fixup_f32 v94, v94, v85, v87
	v_pk_fma_f32 v[96:97], v[48:49], v[96:97], 1.0 op_sel_hi:[1,1,0]
	v_pk_mul_f32 v[90:91], v[94:95], v[90:91] op_sel_hi:[0,1]
	v_pk_mul_f32 v[96:97], v[96:97], v[86:87] op_sel_hi:[1,0]
	v_mov_b32_e32 v87, v1
	v_add_f32_e32 v85, v96, v97
	v_mul_f32_e32 v85, v88, v85
	v_mul_f32_e32 v86, v56, v85
	v_cvt_pk_bf16_f32 v88, v88, v89
	v_cvt_pk_bf16_f32 v89, v94, 0
	v_mov_b32_dpp v87, v86 quad_perm:[1,0,3,2] row_mask:0xf bank_mask:0xf
	v_fmac_f32_e32 v87, v56, v85
	v_cvt_pk_bf16_f32 v90, v90, v91
	v_cvt_pk_bf16_f32 v91, v96, v97
	v_add_f32_dpp v85, v87, v87 quad_perm:[2,3,0,1] row_mask:0xf bank_mask:0xf bound_ctrl:1
	v_lshl_add_u64 v[94:95], v[92:93], 4, s[52:53]
	s_nop 0
	v_add_f32_dpp v85, v85, v85 row_half_mirror row_mask:0xf bank_mask:0xf bound_ctrl:1
	s_nop 1
	v_add_f32_dpp v85, v85, v85 row_mirror row_mask:0xf bank_mask:0xf bound_ctrl:1
	v_mov_b32_e32 v86, v85
	s_nop 1
	v_permlane32_swap_b32 v85, v86
	global_store_dwordx4 v[94:95], v[88:91], off
	v_add_f32_e32 v85, v85, v86
	v_mov_b32_e32 v86, v85
	s_nop 1
	v_permlane16_swap_b32_e32 v85, v86
	v_lshl_add_u64 v[90:91], v[92:93], 1, s[58:59]
	global_store_short_d16_hi v[90:91], v88, off
	s_and_saveexec_b64 s[0:1], s[42:43]
	s_cbranch_execz .LBB0_411
	s_waitcnt lgkmcnt(0)
	v_add_f32_e32 v85, v85, v86
	v_mad_i64_i32 v[86:87], s[22:23], s22, 24, v[114:115]
	global_store_dword v[86:87], v85, off
.LBB0_411:
	s_or_b64 exec, exec, s[0:1]
	s_addk_i32 s21, 0xb00
	v_lshlrev_b32_e32 v89, 16, v83
	v_add_u32_e32 v83, s21, v58
	v_lshlrev_b32_e32 v88, 16, v84
	ds_read_u16 v84, v83 offset:3584
	ds_read_u16 v85, v83 offset:768
	s_waitcnt lgkmcnt(2)
	ds_read_u16 v86, v83 offset:6400
	ds_read_u16 v90, v83 offset:4352
	ds_read_u16 v92, v83 offset:5632
	ds_read_u16 v93, v83 offset:2816
	s_waitcnt lgkmcnt(5)
	v_lshlrev_b32_e32 v84, 16, v84
	s_waitcnt lgkmcnt(3)
	v_lshlrev_b32_e32 v87, 16, v86
	v_lshlrev_b32_e32 v86, 16, v85
	ds_read_u16 v91, v83 offset:1536
	ds_read_u16 v94, v83
	v_pk_add_f32 v[86:87], v[86:87], v[84:85] op_sel_hi:[1,0] neg_lo:[0,1] neg_hi:[0,1]
	ds_read_u16 v83, v83 offset:7168
	v_pk_mul_f32 v[86:87], v[54:55], v[86:87]
	s_waitcnt lgkmcnt(4)
	v_lshlrev_b32_e32 v92, 16, v92
	v_add_f32_e32 v84, v86, v84
	v_add_f32_e32 v84, v84, v87
	v_mul_f32_e32 v85, v0, v84
	s_waitcnt lgkmcnt(2)
	v_lshlrev_b32_e32 v87, 16, v91
	s_waitcnt lgkmcnt(1)
	v_lshlrev_b32_e32 v86, 16, v94
	v_mul_f32_e32 v91, v85, v85
	v_mov_b32_e32 v94, v1
	s_or_b32 s22, s20, s7
	s_nop 0
	v_mov_b32_dpp v94, v91 quad_perm:[1,0,3,2] row_mask:0xf bank_mask:0xf
	v_fmac_f32_e32 v94, v85, v85
	s_nop 1
	v_add_f32_dpp v91, v94, v94 quad_perm:[2,3,0,1] row_mask:0xf bank_mask:0xf bound_ctrl:1
	s_nop 1
	v_add_f32_dpp v91, v91, v91 row_half_mirror row_mask:0xf bank_mask:0xf bound_ctrl:1
	s_nop 1
	v_add_f32_dpp v91, v91, v91 row_mirror row_mask:0xf bank_mask:0xf bound_ctrl:1
	v_mov_b32_e32 v94, v91
	s_nop 1
	v_permlane32_swap_b32 v94, v91
	s_nop 0
	v_add_f32_e32 v94, v94, v91
	v_mov_b32_e32 v95, v94
	s_nop 1
	v_permlane16_swap_b32_e32 v94, v95
	v_lshlrev_b32_e32 v91, 16, v90
	v_lshlrev_b32_e32 v90, 16, v93
	s_waitcnt lgkmcnt(0)
	v_lshlrev_b32_e32 v93, 16, v83
	v_pk_add_f32 v[86:87], v[86:87], v[90:91] neg_lo:[0,1] neg_hi:[0,1]
	s_waitcnt lgkmcnt(0)
	v_add_f32_e32 v83, v94, v95
	v_mul_f32_e32 v94, 0x4f800000, v83
	v_cmp_gt_f32_e32 vcc, s45, v83
	v_pk_fma_f32 v[86:87], v[50:51], v[86:87], v[90:91]
	v_pk_add_f32 v[90:91], v[92:93], v[90:91] neg_lo:[0,1] neg_hi:[0,1]
	v_cndmask_b32_e32 v83, v83, v94, vcc
	v_sqrt_f32_e32 v94, v83
	v_pk_fma_f32 v[86:87], v[52:53], v[90:91], v[86:87]
	v_add_u32_e32 v92, -1, v94
	v_fma_f32 v93, -v92, v94, v83
	v_cmp_ge_f32_e64 s[0:1], 0, v93
	v_add_u32_e32 v93, 1, v94
	s_nop 0
	v_cndmask_b32_e64 v92, v94, v92, s[0:1]
	v_fma_f32 v94, -v93, v94, v83
	v_cmp_lt_f32_e64 s[0:1], 0, v94
	s_nop 1
	v_cndmask_b32_e64 v92, v92, v93, s[0:1]
	v_mul_f32_e32 v93, 0x37800000, v92
	v_cndmask_b32_e32 v92, v92, v93, vcc
	v_cmp_class_f32_e32 vcc, v83, v207
	v_mad_i64_i32 v[90:91], s[0:1], s22, v214, v[46:47]
	s_nop 0
	v_cndmask_b32_e32 v83, v92, v83, vcc
	v_max_f32_e32 v83, 0x2b8cbccc, v83
	v_div_scale_f32 v92, s[0:1], v83, v83, v85
	v_rcp_f32_e32 v93, v92
	s_nop 0
	v_fma_f32 v94, -v92, v93, 1.0
	v_fmac_f32_e32 v93, v94, v93
	v_div_scale_f32 v94, vcc, v85, v83, v85
	v_mul_f32_e32 v95, v94, v93
	v_fma_f32 v96, -v92, v95, v94
	v_fmac_f32_e32 v95, v96, v93
	v_fma_f32 v92, -v92, v95, v94
	v_div_fmas_f32 v92, v92, v93, v95
	v_pk_add_f32 v[94:95], v[88:89], -1.0 op_sel_hi:[1,0]
	v_div_fixup_f32 v92, v92, v83, v85
	v_pk_fma_f32 v[94:95], v[48:49], v[94:95], 1.0 op_sel_hi:[1,1,0]
	v_pk_mul_f32 v[88:89], v[92:93], v[88:89] op_sel_hi:[0,1]
	v_pk_mul_f32 v[94:95], v[94:95], v[84:85] op_sel_hi:[1,0]
	v_mov_b32_e32 v85, v1
	v_add_f32_e32 v83, v94, v95
	v_mul_f32_e32 v83, v86, v83
	v_mul_f32_e32 v84, v56, v83
	v_cvt_pk_bf16_f32 v86, v86, v87
	v_cvt_pk_bf16_f32 v87, v92, 0
	v_mov_b32_dpp v85, v84 quad_perm:[1,0,3,2] row_mask:0xf bank_mask:0xf
	v_fmac_f32_e32 v85, v56, v83
	v_cvt_pk_bf16_f32 v88, v88, v89
	v_cvt_pk_bf16_f32 v89, v94, v95
	v_add_f32_dpp v83, v85, v85 quad_perm:[2,3,0,1] row_mask:0xf bank_mask:0xf bound_ctrl:1
	v_lshl_add_u64 v[92:93], v[90:91], 4, s[52:53]
	s_nop 0
	v_add_f32_dpp v83, v83, v83 row_half_mirror row_mask:0xf bank_mask:0xf bound_ctrl:1
	s_nop 1
	v_add_f32_dpp v83, v83, v83 row_mirror row_mask:0xf bank_mask:0xf bound_ctrl:1
	v_mov_b32_e32 v84, v83
	s_nop 1
	v_permlane32_swap_b32 v84, v83
	global_store_dwordx4 v[92:93], v[86:89], off
	v_add_f32_e32 v83, v84, v83
	v_mov_b32_e32 v84, v83
	s_nop 1
	v_permlane16_swap_b32_e32 v83, v84
	v_lshl_add_u64 v[88:89], v[90:91], 1, s[58:59]
	global_store_short_d16_hi v[88:89], v86, off
	s_and_saveexec_b64 s[0:1], s[42:43]
	s_cbranch_execz .LBB0_413
	s_waitcnt lgkmcnt(0)
	v_add_f32_e32 v83, v83, v84
	v_mad_i64_i32 v[84:85], s[22:23], s22, 24, v[114:115]
	global_store_dword v[84:85], v83, off
.LBB0_413:
	s_or_b64 exec, exec, s[0:1]
	s_addk_i32 s21, 0xb00
	v_lshlrev_b32_e32 v87, 16, v81
	v_add_u32_e32 v81, s21, v58
	v_lshlrev_b32_e32 v86, 16, v82
	ds_read_u16 v82, v81 offset:3584
	ds_read_u16 v83, v81 offset:768
	s_waitcnt lgkmcnt(2)
	ds_read_u16 v84, v81 offset:6400
	ds_read_u16 v88, v81 offset:4352
	ds_read_u16 v90, v81 offset:5632
	ds_read_u16 v91, v81 offset:2816
	s_waitcnt lgkmcnt(5)
	v_lshlrev_b32_e32 v82, 16, v82
	s_waitcnt lgkmcnt(3)
	v_lshlrev_b32_e32 v85, 16, v84
	v_lshlrev_b32_e32 v84, 16, v83
	ds_read_u16 v89, v81 offset:1536
	ds_read_u16 v92, v81
	v_pk_add_f32 v[84:85], v[84:85], v[82:83] op_sel_hi:[1,0] neg_lo:[0,1] neg_hi:[0,1]
	ds_read_u16 v81, v81 offset:7168
	v_pk_mul_f32 v[84:85], v[54:55], v[84:85]
	s_waitcnt lgkmcnt(4)
	v_lshlrev_b32_e32 v90, 16, v90
	v_add_f32_e32 v82, v84, v82
	v_add_f32_e32 v82, v82, v85
	v_mul_f32_e32 v83, v0, v82
	s_waitcnt lgkmcnt(2)
	v_lshlrev_b32_e32 v85, 16, v89
	s_waitcnt lgkmcnt(1)
	v_lshlrev_b32_e32 v84, 16, v92
	v_mul_f32_e32 v89, v83, v83
	v_mov_b32_e32 v92, v1
	s_or_b32 s22, s20, s8
	s_nop 0
	v_mov_b32_dpp v92, v89 quad_perm:[1,0,3,2] row_mask:0xf bank_mask:0xf
	v_fmac_f32_e32 v92, v83, v83
	s_nop 1
	v_add_f32_dpp v89, v92, v92 quad_perm:[2,3,0,1] row_mask:0xf bank_mask:0xf bound_ctrl:1
	s_nop 1
	v_add_f32_dpp v89, v89, v89 row_half_mirror row_mask:0xf bank_mask:0xf bound_ctrl:1
	s_nop 1
	v_add_f32_dpp v89, v89, v89 row_mirror row_mask:0xf bank_mask:0xf bound_ctrl:1
	v_mov_b32_e32 v92, v89
	s_nop 1
	v_permlane32_swap_b32 v89, v92
	s_nop 0
	v_add_f32_e32 v92, v89, v92
	v_mov_b32_e32 v93, v92
	s_nop 1
	v_permlane16_swap_b32_e32 v92, v93
	v_lshlrev_b32_e32 v89, 16, v88
	v_lshlrev_b32_e32 v88, 16, v91
	s_waitcnt lgkmcnt(0)
	v_lshlrev_b32_e32 v91, 16, v81
	v_pk_add_f32 v[84:85], v[84:85], v[88:89] neg_lo:[0,1] neg_hi:[0,1]
	s_waitcnt lgkmcnt(0)
	v_add_f32_e32 v81, v92, v93
	v_mul_f32_e32 v92, 0x4f800000, v81
	v_cmp_gt_f32_e32 vcc, s45, v81
	v_pk_fma_f32 v[84:85], v[50:51], v[84:85], v[88:89]
	v_pk_add_f32 v[88:89], v[90:91], v[88:89] neg_lo:[0,1] neg_hi:[0,1]
	v_cndmask_b32_e32 v81, v81, v92, vcc
	v_sqrt_f32_e32 v92, v81
	v_pk_fma_f32 v[84:85], v[52:53], v[88:89], v[84:85]
	v_add_u32_e32 v90, -1, v92
	v_fma_f32 v91, -v90, v92, v81
	v_cmp_ge_f32_e64 s[0:1], 0, v91
	v_add_u32_e32 v91, 1, v92
	s_nop 0
	v_cndmask_b32_e64 v90, v92, v90, s[0:1]
	v_fma_f32 v92, -v91, v92, v81
	v_cmp_lt_f32_e64 s[0:1], 0, v92
	s_nop 1
	v_cndmask_b32_e64 v90, v90, v91, s[0:1]
	v_mul_f32_e32 v91, 0x37800000, v90
	v_cndmask_b32_e32 v90, v90, v91, vcc
	v_cmp_class_f32_e32 vcc, v81, v207
	v_mad_i64_i32 v[88:89], s[0:1], s22, v214, v[46:47]
	s_nop 0
	v_cndmask_b32_e32 v81, v90, v81, vcc
	v_max_f32_e32 v81, 0x2b8cbccc, v81
	v_div_scale_f32 v90, s[0:1], v81, v81, v83
	v_rcp_f32_e32 v91, v90
	s_nop 0
	v_fma_f32 v92, -v90, v91, 1.0
	v_fmac_f32_e32 v91, v92, v91
	v_div_scale_f32 v92, vcc, v83, v81, v83
	v_mul_f32_e32 v93, v92, v91
	v_fma_f32 v94, -v90, v93, v92
	v_fmac_f32_e32 v93, v94, v91
	v_fma_f32 v90, -v90, v93, v92
	v_div_fmas_f32 v90, v90, v91, v93
	v_pk_add_f32 v[92:93], v[86:87], -1.0 op_sel_hi:[1,0]
	v_div_fixup_f32 v90, v90, v81, v83
	v_pk_fma_f32 v[92:93], v[48:49], v[92:93], 1.0 op_sel_hi:[1,1,0]
	v_pk_mul_f32 v[86:87], v[90:91], v[86:87] op_sel_hi:[0,1]
	v_pk_mul_f32 v[92:93], v[92:93], v[82:83] op_sel_hi:[1,0]
	v_mov_b32_e32 v83, v1
	v_add_f32_e32 v81, v92, v93
	v_mul_f32_e32 v81, v84, v81
	v_mul_f32_e32 v82, v56, v81
	v_cvt_pk_bf16_f32 v84, v84, v85
	v_cvt_pk_bf16_f32 v85, v90, 0
	v_mov_b32_dpp v83, v82 quad_perm:[1,0,3,2] row_mask:0xf bank_mask:0xf
	v_fmac_f32_e32 v83, v56, v81
	v_cvt_pk_bf16_f32 v86, v86, v87
	v_cvt_pk_bf16_f32 v87, v92, v93
	v_add_f32_dpp v81, v83, v83 quad_perm:[2,3,0,1] row_mask:0xf bank_mask:0xf bound_ctrl:1
	v_lshl_add_u64 v[90:91], v[88:89], 4, s[52:53]
	s_nop 0
	v_add_f32_dpp v81, v81, v81 row_half_mirror row_mask:0xf bank_mask:0xf bound_ctrl:1
	s_nop 1
	v_add_f32_dpp v81, v81, v81 row_mirror row_mask:0xf bank_mask:0xf bound_ctrl:1
	v_mov_b32_e32 v82, v81
	s_nop 1
	v_permlane32_swap_b32 v81, v82
	global_store_dwordx4 v[90:91], v[84:87], off
	v_add_f32_e32 v81, v81, v82
	v_mov_b32_e32 v82, v81
	s_nop 1
	v_permlane16_swap_b32_e32 v81, v82
	v_lshl_add_u64 v[86:87], v[88:89], 1, s[58:59]
	global_store_short_d16_hi v[86:87], v84, off
	s_and_saveexec_b64 s[0:1], s[42:43]
	s_cbranch_execz .LBB0_415
	s_waitcnt lgkmcnt(0)
	v_add_f32_e32 v81, v81, v82
	v_mad_i64_i32 v[82:83], s[22:23], s22, 24, v[114:115]
	global_store_dword v[82:83], v81, off
.LBB0_415:
	s_or_b64 exec, exec, s[0:1]
	s_addk_i32 s21, 0xb00
	v_lshlrev_b32_e32 v85, 16, v79
	v_add_u32_e32 v79, s21, v58
	v_lshlrev_b32_e32 v84, 16, v80
	ds_read_u16 v80, v79 offset:3584
	ds_read_u16 v81, v79 offset:768
	s_waitcnt lgkmcnt(2)
	ds_read_u16 v82, v79 offset:6400
	ds_read_u16 v86, v79 offset:4352
	ds_read_u16 v88, v79 offset:5632
	ds_read_u16 v89, v79 offset:2816
	s_waitcnt lgkmcnt(5)
	v_lshlrev_b32_e32 v80, 16, v80
	s_waitcnt lgkmcnt(3)
	v_lshlrev_b32_e32 v83, 16, v82
	v_lshlrev_b32_e32 v82, 16, v81
	ds_read_u16 v87, v79 offset:1536
	ds_read_u16 v90, v79
	v_pk_add_f32 v[82:83], v[82:83], v[80:81] op_sel_hi:[1,0] neg_lo:[0,1] neg_hi:[0,1]
	ds_read_u16 v79, v79 offset:7168
	v_pk_mul_f32 v[82:83], v[54:55], v[82:83]
	s_waitcnt lgkmcnt(4)
	v_lshlrev_b32_e32 v88, 16, v88
	v_add_f32_e32 v80, v82, v80
	v_add_f32_e32 v80, v80, v83
	v_mul_f32_e32 v81, v0, v80
	s_waitcnt lgkmcnt(2)
	v_lshlrev_b32_e32 v83, 16, v87
	s_waitcnt lgkmcnt(1)
	v_lshlrev_b32_e32 v82, 16, v90
	v_mul_f32_e32 v87, v81, v81
	v_mov_b32_e32 v90, v1
	s_or_b32 s22, s20, s9
	s_nop 0
	v_mov_b32_dpp v90, v87 quad_perm:[1,0,3,2] row_mask:0xf bank_mask:0xf
	v_fmac_f32_e32 v90, v81, v81
	s_nop 1
	v_add_f32_dpp v87, v90, v90 quad_perm:[2,3,0,1] row_mask:0xf bank_mask:0xf bound_ctrl:1
	s_nop 1
	v_add_f32_dpp v87, v87, v87 row_half_mirror row_mask:0xf bank_mask:0xf bound_ctrl:1
	s_nop 1
	v_add_f32_dpp v87, v87, v87 row_mirror row_mask:0xf bank_mask:0xf bound_ctrl:1
	v_mov_b32_e32 v90, v87
	s_nop 1
	v_permlane32_swap_b32 v87, v90
	s_nop 0
	v_add_f32_e32 v90, v87, v90
	v_mov_b32_e32 v91, v90
	s_nop 1
	v_permlane16_swap_b32_e32 v90, v91
	v_lshlrev_b32_e32 v87, 16, v86
	v_lshlrev_b32_e32 v86, 16, v89
	s_waitcnt lgkmcnt(0)
	v_lshlrev_b32_e32 v89, 16, v79
	v_pk_add_f32 v[82:83], v[82:83], v[86:87] neg_lo:[0,1] neg_hi:[0,1]
	s_waitcnt lgkmcnt(0)
	v_add_f32_e32 v79, v90, v91
	v_mul_f32_e32 v90, 0x4f800000, v79
	v_cmp_gt_f32_e32 vcc, s45, v79
	v_pk_fma_f32 v[82:83], v[50:51], v[82:83], v[86:87]
	v_pk_add_f32 v[86:87], v[88:89], v[86:87] neg_lo:[0,1] neg_hi:[0,1]
	v_cndmask_b32_e32 v79, v79, v90, vcc
	v_sqrt_f32_e32 v90, v79
	v_pk_fma_f32 v[82:83], v[52:53], v[86:87], v[82:83]
	v_add_u32_e32 v88, -1, v90
	v_fma_f32 v89, -v88, v90, v79
	v_cmp_ge_f32_e64 s[0:1], 0, v89
	v_add_u32_e32 v89, 1, v90
	s_nop 0
	v_cndmask_b32_e64 v88, v90, v88, s[0:1]
	v_fma_f32 v90, -v89, v90, v79
	v_cmp_lt_f32_e64 s[0:1], 0, v90
	s_nop 1
	v_cndmask_b32_e64 v88, v88, v89, s[0:1]
	v_mul_f32_e32 v89, 0x37800000, v88
	v_cndmask_b32_e32 v88, v88, v89, vcc
	v_cmp_class_f32_e32 vcc, v79, v207
	v_mad_i64_i32 v[86:87], s[0:1], s22, v214, v[46:47]
	s_nop 0
	v_cndmask_b32_e32 v79, v88, v79, vcc
	v_max_f32_e32 v79, 0x2b8cbccc, v79
	v_div_scale_f32 v88, s[0:1], v79, v79, v81
	v_rcp_f32_e32 v89, v88
	s_nop 0
	v_fma_f32 v90, -v88, v89, 1.0
	v_fmac_f32_e32 v89, v90, v89
	v_div_scale_f32 v90, vcc, v81, v79, v81
	v_mul_f32_e32 v91, v90, v89
	v_fma_f32 v92, -v88, v91, v90
	v_fmac_f32_e32 v91, v92, v89
	v_fma_f32 v88, -v88, v91, v90
	v_div_fmas_f32 v88, v88, v89, v91
	v_pk_add_f32 v[90:91], v[84:85], -1.0 op_sel_hi:[1,0]
	v_div_fixup_f32 v88, v88, v79, v81
	v_pk_fma_f32 v[90:91], v[48:49], v[90:91], 1.0 op_sel_hi:[1,1,0]
	v_pk_mul_f32 v[84:85], v[88:89], v[84:85] op_sel_hi:[0,1]
	v_pk_mul_f32 v[90:91], v[90:91], v[80:81] op_sel_hi:[1,0]
	v_mov_b32_e32 v81, v1
	v_add_f32_e32 v79, v90, v91
	v_mul_f32_e32 v79, v82, v79
	v_mul_f32_e32 v80, v56, v79
	v_cvt_pk_bf16_f32 v82, v82, v83
	v_cvt_pk_bf16_f32 v83, v88, 0
	v_mov_b32_dpp v81, v80 quad_perm:[1,0,3,2] row_mask:0xf bank_mask:0xf
	v_fmac_f32_e32 v81, v56, v79
	v_cvt_pk_bf16_f32 v84, v84, v85
	v_cvt_pk_bf16_f32 v85, v90, v91
	v_add_f32_dpp v79, v81, v81 quad_perm:[2,3,0,1] row_mask:0xf bank_mask:0xf bound_ctrl:1
	v_lshl_add_u64 v[88:89], v[86:87], 4, s[52:53]
	s_nop 0
	v_add_f32_dpp v79, v79, v79 row_half_mirror row_mask:0xf bank_mask:0xf bound_ctrl:1
	s_nop 1
	v_add_f32_dpp v79, v79, v79 row_mirror row_mask:0xf bank_mask:0xf bound_ctrl:1
	v_mov_b32_e32 v80, v79
	s_nop 1
	v_permlane32_swap_b32 v79, v80
	global_store_dwordx4 v[88:89], v[82:85], off
	v_add_f32_e32 v79, v79, v80
	v_mov_b32_e32 v80, v79
	s_nop 1
	v_permlane16_swap_b32_e32 v79, v80
	v_lshl_add_u64 v[84:85], v[86:87], 1, s[58:59]
	global_store_short_d16_hi v[84:85], v82, off
	s_and_saveexec_b64 s[0:1], s[42:43]
	s_cbranch_execz .LBB0_417
	s_waitcnt lgkmcnt(0)
	v_add_f32_e32 v79, v79, v80
	v_mad_i64_i32 v[80:81], s[22:23], s22, 24, v[114:115]
	global_store_dword v[80:81], v79, off
.LBB0_417:
	s_or_b64 exec, exec, s[0:1]
	s_addk_i32 s21, 0xb00
	v_lshlrev_b32_e32 v83, 16, v77
	v_add_u32_e32 v77, s21, v58
	v_lshlrev_b32_e32 v82, 16, v78
	ds_read_u16 v78, v77 offset:3584
	ds_read_u16 v79, v77 offset:768
	s_waitcnt lgkmcnt(2)
	ds_read_u16 v80, v77 offset:6400
	ds_read_u16 v84, v77 offset:4352
	ds_read_u16 v86, v77 offset:5632
	ds_read_u16 v87, v77 offset:2816
	s_waitcnt lgkmcnt(5)
	v_lshlrev_b32_e32 v78, 16, v78
	s_waitcnt lgkmcnt(3)
	v_lshlrev_b32_e32 v81, 16, v80
	v_lshlrev_b32_e32 v80, 16, v79
	ds_read_u16 v85, v77 offset:1536
	ds_read_u16 v88, v77
	v_pk_add_f32 v[80:81], v[80:81], v[78:79] op_sel_hi:[1,0] neg_lo:[0,1] neg_hi:[0,1]
	ds_read_u16 v77, v77 offset:7168
	v_pk_mul_f32 v[80:81], v[54:55], v[80:81]
	s_waitcnt lgkmcnt(4)
	v_lshlrev_b32_e32 v86, 16, v86
	v_add_f32_e32 v78, v80, v78
	v_add_f32_e32 v78, v78, v81
	v_mul_f32_e32 v79, v0, v78
	s_waitcnt lgkmcnt(2)
	v_lshlrev_b32_e32 v81, 16, v85
	s_waitcnt lgkmcnt(1)
	v_lshlrev_b32_e32 v80, 16, v88
	v_mul_f32_e32 v85, v79, v79
	v_mov_b32_e32 v88, v1
	s_or_b32 s22, s20, s10
	s_nop 0
	v_mov_b32_dpp v88, v85 quad_perm:[1,0,3,2] row_mask:0xf bank_mask:0xf
	v_fmac_f32_e32 v88, v79, v79
	s_nop 1
	v_add_f32_dpp v85, v88, v88 quad_perm:[2,3,0,1] row_mask:0xf bank_mask:0xf bound_ctrl:1
	s_nop 1
	v_add_f32_dpp v85, v85, v85 row_half_mirror row_mask:0xf bank_mask:0xf bound_ctrl:1
	s_nop 1
	v_add_f32_dpp v85, v85, v85 row_mirror row_mask:0xf bank_mask:0xf bound_ctrl:1
	v_mov_b32_e32 v88, v85
	s_nop 1
	v_permlane32_swap_b32 v85, v88
	s_nop 0
	v_add_f32_e32 v88, v85, v88
	v_mov_b32_e32 v89, v88
	s_nop 1
	v_permlane16_swap_b32_e32 v88, v89
	v_lshlrev_b32_e32 v85, 16, v84
	v_lshlrev_b32_e32 v84, 16, v87
	s_waitcnt lgkmcnt(0)
	v_lshlrev_b32_e32 v87, 16, v77
	v_pk_add_f32 v[80:81], v[80:81], v[84:85] neg_lo:[0,1] neg_hi:[0,1]
	s_waitcnt lgkmcnt(0)
	v_add_f32_e32 v77, v88, v89
	v_mul_f32_e32 v88, 0x4f800000, v77
	v_cmp_gt_f32_e32 vcc, s45, v77
	v_pk_fma_f32 v[80:81], v[50:51], v[80:81], v[84:85]
	v_pk_add_f32 v[84:85], v[86:87], v[84:85] neg_lo:[0,1] neg_hi:[0,1]
	v_cndmask_b32_e32 v77, v77, v88, vcc
	v_sqrt_f32_e32 v88, v77
	v_pk_fma_f32 v[80:81], v[52:53], v[84:85], v[80:81]
	v_add_u32_e32 v86, -1, v88
	v_fma_f32 v87, -v86, v88, v77
	v_cmp_ge_f32_e64 s[0:1], 0, v87
	v_add_u32_e32 v87, 1, v88
	s_nop 0
	v_cndmask_b32_e64 v86, v88, v86, s[0:1]
	v_fma_f32 v88, -v87, v88, v77
	v_cmp_lt_f32_e64 s[0:1], 0, v88
	s_nop 1
	v_cndmask_b32_e64 v86, v86, v87, s[0:1]
	v_mul_f32_e32 v87, 0x37800000, v86
	v_cndmask_b32_e32 v86, v86, v87, vcc
	v_cmp_class_f32_e32 vcc, v77, v207
	v_mad_i64_i32 v[84:85], s[0:1], s22, v214, v[46:47]
	s_nop 0
	v_cndmask_b32_e32 v77, v86, v77, vcc
	v_max_f32_e32 v77, 0x2b8cbccc, v77
	v_div_scale_f32 v86, s[0:1], v77, v77, v79
	v_rcp_f32_e32 v87, v86
	s_nop 0
	v_fma_f32 v88, -v86, v87, 1.0
	v_fmac_f32_e32 v87, v88, v87
	v_div_scale_f32 v88, vcc, v79, v77, v79
	v_mul_f32_e32 v89, v88, v87
	v_fma_f32 v90, -v86, v89, v88
	v_fmac_f32_e32 v89, v90, v87
	v_fma_f32 v86, -v86, v89, v88
	v_div_fmas_f32 v86, v86, v87, v89
	v_pk_add_f32 v[88:89], v[82:83], -1.0 op_sel_hi:[1,0]
	v_div_fixup_f32 v86, v86, v77, v79
	v_pk_fma_f32 v[88:89], v[48:49], v[88:89], 1.0 op_sel_hi:[1,1,0]
	v_pk_mul_f32 v[82:83], v[86:87], v[82:83] op_sel_hi:[0,1]
	v_pk_mul_f32 v[88:89], v[88:89], v[78:79] op_sel_hi:[1,0]
	v_mov_b32_e32 v79, v1
	v_add_f32_e32 v77, v88, v89
	v_mul_f32_e32 v77, v80, v77
	v_mul_f32_e32 v78, v56, v77
	v_cvt_pk_bf16_f32 v80, v80, v81
	v_cvt_pk_bf16_f32 v81, v86, 0
	v_mov_b32_dpp v79, v78 quad_perm:[1,0,3,2] row_mask:0xf bank_mask:0xf
	v_fmac_f32_e32 v79, v56, v77
	v_cvt_pk_bf16_f32 v82, v82, v83
	v_cvt_pk_bf16_f32 v83, v88, v89
	v_add_f32_dpp v77, v79, v79 quad_perm:[2,3,0,1] row_mask:0xf bank_mask:0xf bound_ctrl:1
	v_lshl_add_u64 v[86:87], v[84:85], 4, s[52:53]
	s_nop 0
	v_add_f32_dpp v77, v77, v77 row_half_mirror row_mask:0xf bank_mask:0xf bound_ctrl:1
	s_nop 1
	v_add_f32_dpp v77, v77, v77 row_mirror row_mask:0xf bank_mask:0xf bound_ctrl:1
	v_mov_b32_e32 v78, v77
	s_nop 1
	v_permlane32_swap_b32 v77, v78
	global_store_dwordx4 v[86:87], v[80:83], off
	v_add_f32_e32 v77, v77, v78
	v_mov_b32_e32 v78, v77
	s_nop 1
	v_permlane16_swap_b32_e32 v77, v78
	v_lshl_add_u64 v[82:83], v[84:85], 1, s[58:59]
	global_store_short_d16_hi v[82:83], v80, off
	s_and_saveexec_b64 s[0:1], s[42:43]
	s_cbranch_execz .LBB0_419
	s_waitcnt lgkmcnt(0)
	v_add_f32_e32 v77, v77, v78
	v_mad_i64_i32 v[78:79], s[22:23], s22, 24, v[114:115]
	global_store_dword v[78:79], v77, off
.LBB0_419:
	s_or_b64 exec, exec, s[0:1]
	s_addk_i32 s21, 0xb00
	v_lshlrev_b32_e32 v80, 16, v75
	v_add_u32_e32 v75, s21, v58
	v_lshlrev_b32_e32 v81, 16, v76
	ds_read_u16 v76, v75 offset:3584
	ds_read_u16 v77, v75 offset:768
	s_waitcnt lgkmcnt(2)
	ds_read_u16 v78, v75 offset:6400
	ds_read_u16 v82, v75 offset:4352
	ds_read_u16 v84, v75 offset:5632
	ds_read_u16 v85, v75 offset:2816
	s_waitcnt lgkmcnt(5)
	v_lshlrev_b32_e32 v76, 16, v76
	s_waitcnt lgkmcnt(3)
	v_lshlrev_b32_e32 v79, 16, v78
	v_lshlrev_b32_e32 v78, 16, v77
	ds_read_u16 v83, v75 offset:1536
	ds_read_u16 v86, v75
	v_pk_add_f32 v[78:79], v[78:79], v[76:77] op_sel_hi:[1,0] neg_lo:[0,1] neg_hi:[0,1]
	ds_read_u16 v75, v75 offset:7168
	v_pk_mul_f32 v[78:79], v[54:55], v[78:79]
	s_waitcnt lgkmcnt(4)
	v_lshlrev_b32_e32 v84, 16, v84
	v_add_f32_e32 v76, v78, v76
	v_add_f32_e32 v76, v76, v79
	v_mul_f32_e32 v77, v0, v76
	s_waitcnt lgkmcnt(2)
	v_lshlrev_b32_e32 v79, 16, v83
	s_waitcnt lgkmcnt(1)
	v_lshlrev_b32_e32 v78, 16, v86
	v_mul_f32_e32 v83, v77, v77
	v_mov_b32_e32 v86, v1
	s_or_b32 s22, s20, s11
	s_nop 0
	v_mov_b32_dpp v86, v83 quad_perm:[1,0,3,2] row_mask:0xf bank_mask:0xf
	v_fmac_f32_e32 v86, v77, v77
	s_nop 1
	v_add_f32_dpp v83, v86, v86 quad_perm:[2,3,0,1] row_mask:0xf bank_mask:0xf bound_ctrl:1
	s_nop 1
	v_add_f32_dpp v83, v83, v83 row_half_mirror row_mask:0xf bank_mask:0xf bound_ctrl:1
	s_nop 1
	v_add_f32_dpp v83, v83, v83 row_mirror row_mask:0xf bank_mask:0xf bound_ctrl:1
	v_mov_b32_e32 v86, v83
	s_nop 1
	v_permlane32_swap_b32 v86, v83
	s_nop 0
	v_add_f32_e32 v86, v86, v83
	v_mov_b32_e32 v87, v86
	s_nop 1
	v_permlane16_swap_b32_e32 v86, v87
	v_lshlrev_b32_e32 v83, 16, v82
	v_lshlrev_b32_e32 v82, 16, v85
	s_waitcnt lgkmcnt(0)
	v_lshlrev_b32_e32 v85, 16, v75
	v_pk_add_f32 v[78:79], v[78:79], v[82:83] neg_lo:[0,1] neg_hi:[0,1]
	s_waitcnt lgkmcnt(0)
	v_add_f32_e32 v75, v86, v87
	v_mul_f32_e32 v86, 0x4f800000, v75
	v_cmp_gt_f32_e32 vcc, s45, v75
	v_pk_fma_f32 v[78:79], v[50:51], v[78:79], v[82:83]
	v_pk_add_f32 v[82:83], v[84:85], v[82:83] neg_lo:[0,1] neg_hi:[0,1]
	v_cndmask_b32_e32 v75, v75, v86, vcc
	v_sqrt_f32_e32 v86, v75
	v_pk_fma_f32 v[78:79], v[52:53], v[82:83], v[78:79]
	v_add_u32_e32 v84, -1, v86
	v_fma_f32 v85, -v84, v86, v75
	v_cmp_ge_f32_e64 s[0:1], 0, v85
	v_add_u32_e32 v85, 1, v86
	s_nop 0
	v_cndmask_b32_e64 v84, v86, v84, s[0:1]
	v_fma_f32 v86, -v85, v86, v75
	v_cmp_lt_f32_e64 s[0:1], 0, v86
	s_nop 1
	v_cndmask_b32_e64 v84, v84, v85, s[0:1]
	v_mul_f32_e32 v85, 0x37800000, v84
	v_cndmask_b32_e32 v84, v84, v85, vcc
	v_cmp_class_f32_e32 vcc, v75, v207
	v_mad_i64_i32 v[82:83], s[0:1], s22, v214, v[46:47]
	s_nop 0
	v_cndmask_b32_e32 v75, v84, v75, vcc
	v_max_f32_e32 v75, 0x2b8cbccc, v75
	v_div_scale_f32 v84, s[0:1], v75, v75, v77
	v_rcp_f32_e32 v85, v84
	s_nop 0
	v_fma_f32 v86, -v84, v85, 1.0
	v_fmac_f32_e32 v85, v86, v85
	v_div_scale_f32 v86, vcc, v77, v75, v77
	v_mul_f32_e32 v87, v86, v85
	v_fma_f32 v88, -v84, v87, v86
	v_fmac_f32_e32 v87, v88, v85
	v_fma_f32 v84, -v84, v87, v86
	v_div_fmas_f32 v84, v84, v85, v87
	v_pk_add_f32 v[86:87], v[80:81], -1.0 op_sel_hi:[1,0]
	v_div_fixup_f32 v84, v84, v75, v77
	v_pk_fma_f32 v[86:87], v[48:49], v[86:87], 1.0 op_sel_hi:[1,1,0]
	v_pk_mul_f32 v[80:81], v[84:85], v[80:81] op_sel_hi:[0,1]
	v_pk_mul_f32 v[86:87], v[86:87], v[76:77] op_sel_hi:[1,0]
	v_mov_b32_e32 v77, v1
	v_add_f32_e32 v75, v86, v87
	v_mul_f32_e32 v75, v78, v75
	v_mul_f32_e32 v76, v56, v75
	v_cvt_pk_bf16_f32 v78, v78, v79
	v_cvt_pk_bf16_f32 v79, v84, 0
	v_mov_b32_dpp v77, v76 quad_perm:[1,0,3,2] row_mask:0xf bank_mask:0xf
	v_fmac_f32_e32 v77, v56, v75
	v_cvt_pk_bf16_f32 v80, v80, v81
	v_cvt_pk_bf16_f32 v81, v86, v87
	v_add_f32_dpp v75, v77, v77 quad_perm:[2,3,0,1] row_mask:0xf bank_mask:0xf bound_ctrl:1
	v_lshl_add_u64 v[84:85], v[82:83], 4, s[52:53]
	s_nop 0
	v_add_f32_dpp v75, v75, v75 row_half_mirror row_mask:0xf bank_mask:0xf bound_ctrl:1
	s_nop 1
	v_add_f32_dpp v75, v75, v75 row_mirror row_mask:0xf bank_mask:0xf bound_ctrl:1
	v_mov_b32_e32 v76, v75
	s_nop 1
	v_permlane32_swap_b32 v76, v75
	global_store_dwordx4 v[84:85], v[78:81], off
	v_add_f32_e32 v75, v76, v75
	v_mov_b32_e32 v76, v75
	s_nop 1
	v_permlane16_swap_b32_e32 v75, v76
	v_lshl_add_u64 v[80:81], v[82:83], 1, s[58:59]
	global_store_short_d16_hi v[80:81], v78, off
	s_and_saveexec_b64 s[0:1], s[42:43]
	s_cbranch_execz .LBB0_421
	s_waitcnt lgkmcnt(0)
	v_add_f32_e32 v75, v75, v76
	v_mad_i64_i32 v[76:77], s[22:23], s22, 24, v[114:115]
	global_store_dword v[76:77], v75, off
.LBB0_421:
	s_or_b64 exec, exec, s[0:1]
	s_addk_i32 s21, 0xb00
	v_lshlrev_b32_e32 v78, 16, v73
	v_add_u32_e32 v73, s21, v58
	v_lshlrev_b32_e32 v79, 16, v74
	ds_read_u16 v74, v73 offset:3584
	ds_read_u16 v75, v73 offset:768
	s_waitcnt lgkmcnt(2)
	ds_read_u16 v76, v73 offset:6400
	ds_read_u16 v80, v73 offset:4352
	ds_read_u16 v82, v73 offset:5632
	ds_read_u16 v83, v73 offset:2816
	s_waitcnt lgkmcnt(5)
	v_lshlrev_b32_e32 v74, 16, v74
	s_waitcnt lgkmcnt(3)
	v_lshlrev_b32_e32 v77, 16, v76
	v_lshlrev_b32_e32 v76, 16, v75
	ds_read_u16 v81, v73 offset:1536
	ds_read_u16 v84, v73
	v_pk_add_f32 v[76:77], v[76:77], v[74:75] op_sel_hi:[1,0] neg_lo:[0,1] neg_hi:[0,1]
	ds_read_u16 v73, v73 offset:7168
	v_pk_mul_f32 v[76:77], v[54:55], v[76:77]
	s_waitcnt lgkmcnt(4)
	v_lshlrev_b32_e32 v82, 16, v82
	v_add_f32_e32 v74, v76, v74
	v_add_f32_e32 v74, v74, v77
	v_mul_f32_e32 v75, v0, v74
	s_waitcnt lgkmcnt(2)
	v_lshlrev_b32_e32 v77, 16, v81
	s_waitcnt lgkmcnt(1)
	v_lshlrev_b32_e32 v76, 16, v84
	v_mul_f32_e32 v81, v75, v75
	v_mov_b32_e32 v84, v1
	s_or_b32 s22, s20, s12
	s_nop 0
	v_mov_b32_dpp v84, v81 quad_perm:[1,0,3,2] row_mask:0xf bank_mask:0xf
	v_fmac_f32_e32 v84, v75, v75
	s_nop 1
	v_add_f32_dpp v81, v84, v84 quad_perm:[2,3,0,1] row_mask:0xf bank_mask:0xf bound_ctrl:1
	s_nop 1
	v_add_f32_dpp v81, v81, v81 row_half_mirror row_mask:0xf bank_mask:0xf bound_ctrl:1
	s_nop 1
	v_add_f32_dpp v81, v81, v81 row_mirror row_mask:0xf bank_mask:0xf bound_ctrl:1
	v_mov_b32_e32 v84, v81
	s_nop 1
	v_permlane32_swap_b32 v81, v84
	s_nop 0
	v_add_f32_e32 v84, v81, v84
	v_mov_b32_e32 v85, v84
	s_nop 1
	v_permlane16_swap_b32_e32 v84, v85
	v_lshlrev_b32_e32 v81, 16, v80
	v_lshlrev_b32_e32 v80, 16, v83
	s_waitcnt lgkmcnt(0)
	v_lshlrev_b32_e32 v83, 16, v73
	v_pk_add_f32 v[76:77], v[76:77], v[80:81] neg_lo:[0,1] neg_hi:[0,1]
	s_waitcnt lgkmcnt(0)
	v_add_f32_e32 v73, v84, v85
	v_mul_f32_e32 v84, 0x4f800000, v73
	v_cmp_gt_f32_e32 vcc, s45, v73
	v_pk_fma_f32 v[76:77], v[50:51], v[76:77], v[80:81]
	v_pk_add_f32 v[80:81], v[82:83], v[80:81] neg_lo:[0,1] neg_hi:[0,1]
	v_cndmask_b32_e32 v73, v73, v84, vcc
	v_sqrt_f32_e32 v84, v73
	v_pk_fma_f32 v[76:77], v[52:53], v[80:81], v[76:77]
	v_add_u32_e32 v82, -1, v84
	v_fma_f32 v83, -v82, v84, v73
	v_cmp_ge_f32_e64 s[0:1], 0, v83
	v_add_u32_e32 v83, 1, v84
	s_nop 0
	v_cndmask_b32_e64 v82, v84, v82, s[0:1]
	v_fma_f32 v84, -v83, v84, v73
	v_cmp_lt_f32_e64 s[0:1], 0, v84
	s_nop 1
	v_cndmask_b32_e64 v82, v82, v83, s[0:1]
	v_mul_f32_e32 v83, 0x37800000, v82
	v_cndmask_b32_e32 v82, v82, v83, vcc
	v_cmp_class_f32_e32 vcc, v73, v207
	v_mad_i64_i32 v[80:81], s[0:1], s22, v214, v[46:47]
	s_nop 0
	v_cndmask_b32_e32 v73, v82, v73, vcc
	v_max_f32_e32 v73, 0x2b8cbccc, v73
	v_div_scale_f32 v82, s[0:1], v73, v73, v75
	v_rcp_f32_e32 v83, v82
	s_nop 0
	v_fma_f32 v84, -v82, v83, 1.0
	v_fmac_f32_e32 v83, v84, v83
	v_div_scale_f32 v84, vcc, v75, v73, v75
	v_mul_f32_e32 v85, v84, v83
	v_fma_f32 v86, -v82, v85, v84
	v_fmac_f32_e32 v85, v86, v83
	v_fma_f32 v82, -v82, v85, v84
	v_div_fmas_f32 v82, v82, v83, v85
	v_pk_add_f32 v[84:85], v[78:79], -1.0 op_sel_hi:[1,0]
	v_div_fixup_f32 v82, v82, v73, v75
	v_pk_fma_f32 v[84:85], v[48:49], v[84:85], 1.0 op_sel_hi:[1,1,0]
	v_pk_mul_f32 v[78:79], v[82:83], v[78:79] op_sel_hi:[0,1]
	v_pk_mul_f32 v[84:85], v[84:85], v[74:75] op_sel_hi:[1,0]
	v_mov_b32_e32 v75, v1
	v_add_f32_e32 v73, v84, v85
	v_mul_f32_e32 v73, v76, v73
	v_mul_f32_e32 v74, v56, v73
	v_cvt_pk_bf16_f32 v76, v76, v77
	v_cvt_pk_bf16_f32 v77, v82, 0
	v_mov_b32_dpp v75, v74 quad_perm:[1,0,3,2] row_mask:0xf bank_mask:0xf
	v_fmac_f32_e32 v75, v56, v73
	v_cvt_pk_bf16_f32 v78, v78, v79
	v_cvt_pk_bf16_f32 v79, v84, v85
	v_add_f32_dpp v73, v75, v75 quad_perm:[2,3,0,1] row_mask:0xf bank_mask:0xf bound_ctrl:1
	v_lshl_add_u64 v[82:83], v[80:81], 4, s[52:53]
	s_nop 0
	v_add_f32_dpp v73, v73, v73 row_half_mirror row_mask:0xf bank_mask:0xf bound_ctrl:1
	s_nop 1
	v_add_f32_dpp v73, v73, v73 row_mirror row_mask:0xf bank_mask:0xf bound_ctrl:1
	v_mov_b32_e32 v74, v73
	s_nop 1
	v_permlane32_swap_b32 v73, v74
	global_store_dwordx4 v[82:83], v[76:79], off
	v_add_f32_e32 v73, v73, v74
	v_mov_b32_e32 v74, v73
	s_nop 1
	v_permlane16_swap_b32_e32 v73, v74
	v_lshl_add_u64 v[78:79], v[80:81], 1, s[58:59]
	global_store_short_d16_hi v[78:79], v76, off
	s_and_saveexec_b64 s[0:1], s[42:43]
	s_cbranch_execz .LBB0_423
	s_waitcnt lgkmcnt(0)
	v_add_f32_e32 v73, v73, v74
	v_mad_i64_i32 v[74:75], s[22:23], s22, 24, v[114:115]
	global_store_dword v[74:75], v73, off
.LBB0_423:
	s_or_b64 exec, exec, s[0:1]
	s_addk_i32 s21, 0xb00
	v_lshlrev_b32_e32 v76, 16, v71
	v_add_u32_e32 v71, s21, v58
	v_lshlrev_b32_e32 v77, 16, v72
	ds_read_u16 v72, v71 offset:3584
	ds_read_u16 v73, v71 offset:768
	s_waitcnt lgkmcnt(2)
	ds_read_u16 v74, v71 offset:6400
	ds_read_u16 v78, v71 offset:4352
	ds_read_u16 v80, v71 offset:5632
	ds_read_u16 v81, v71 offset:2816
	s_waitcnt lgkmcnt(5)
	v_lshlrev_b32_e32 v72, 16, v72
	s_waitcnt lgkmcnt(3)
	v_lshlrev_b32_e32 v75, 16, v74
	v_lshlrev_b32_e32 v74, 16, v73
	ds_read_u16 v79, v71 offset:1536
	ds_read_u16 v82, v71
	v_pk_add_f32 v[74:75], v[74:75], v[72:73] op_sel_hi:[1,0] neg_lo:[0,1] neg_hi:[0,1]
	ds_read_u16 v71, v71 offset:7168
	v_pk_mul_f32 v[74:75], v[54:55], v[74:75]
	s_waitcnt lgkmcnt(4)
	v_lshlrev_b32_e32 v80, 16, v80
	v_add_f32_e32 v72, v74, v72
	v_add_f32_e32 v72, v72, v75
	v_mul_f32_e32 v73, v0, v72
	s_waitcnt lgkmcnt(2)
	v_lshlrev_b32_e32 v75, 16, v79
	s_waitcnt lgkmcnt(1)
	v_lshlrev_b32_e32 v74, 16, v82
	v_mul_f32_e32 v79, v73, v73
	v_mov_b32_e32 v82, v1
	s_or_b32 s22, s20, s13
	s_nop 0
	v_mov_b32_dpp v82, v79 quad_perm:[1,0,3,2] row_mask:0xf bank_mask:0xf
	v_fmac_f32_e32 v82, v73, v73
	s_nop 1
	v_add_f32_dpp v79, v82, v82 quad_perm:[2,3,0,1] row_mask:0xf bank_mask:0xf bound_ctrl:1
	s_nop 1
	v_add_f32_dpp v79, v79, v79 row_half_mirror row_mask:0xf bank_mask:0xf bound_ctrl:1
	s_nop 1
	v_add_f32_dpp v79, v79, v79 row_mirror row_mask:0xf bank_mask:0xf bound_ctrl:1
	v_mov_b32_e32 v82, v79
	s_nop 1
	v_permlane32_swap_b32 v79, v82
	s_nop 0
	v_add_f32_e32 v82, v79, v82
	v_mov_b32_e32 v83, v82
	s_nop 1
	v_permlane16_swap_b32_e32 v82, v83
	v_lshlrev_b32_e32 v79, 16, v78
	v_lshlrev_b32_e32 v78, 16, v81
	s_waitcnt lgkmcnt(0)
	v_lshlrev_b32_e32 v81, 16, v71
	v_pk_add_f32 v[74:75], v[74:75], v[78:79] neg_lo:[0,1] neg_hi:[0,1]
	s_waitcnt lgkmcnt(0)
	v_add_f32_e32 v71, v82, v83
	v_mul_f32_e32 v82, 0x4f800000, v71
	v_cmp_gt_f32_e32 vcc, s45, v71
	v_pk_fma_f32 v[74:75], v[50:51], v[74:75], v[78:79]
	v_pk_add_f32 v[78:79], v[80:81], v[78:79] neg_lo:[0,1] neg_hi:[0,1]
	v_cndmask_b32_e32 v71, v71, v82, vcc
	v_sqrt_f32_e32 v82, v71
	v_pk_fma_f32 v[74:75], v[52:53], v[78:79], v[74:75]
	v_add_u32_e32 v80, -1, v82
	v_fma_f32 v81, -v80, v82, v71
	v_cmp_ge_f32_e64 s[0:1], 0, v81
	v_add_u32_e32 v81, 1, v82
	s_nop 0
	v_cndmask_b32_e64 v80, v82, v80, s[0:1]
	v_fma_f32 v82, -v81, v82, v71
	v_cmp_lt_f32_e64 s[0:1], 0, v82
	s_nop 1
	v_cndmask_b32_e64 v80, v80, v81, s[0:1]
	v_mul_f32_e32 v81, 0x37800000, v80
	v_cndmask_b32_e32 v80, v80, v81, vcc
	v_cmp_class_f32_e32 vcc, v71, v207
	v_mad_i64_i32 v[78:79], s[0:1], s22, v214, v[46:47]
	s_nop 0
	v_cndmask_b32_e32 v71, v80, v71, vcc
	v_max_f32_e32 v71, 0x2b8cbccc, v71
	v_div_scale_f32 v80, s[0:1], v71, v71, v73
	v_rcp_f32_e32 v81, v80
	s_nop 0
	v_fma_f32 v82, -v80, v81, 1.0
	v_fmac_f32_e32 v81, v82, v81
	v_div_scale_f32 v82, vcc, v73, v71, v73
	v_mul_f32_e32 v83, v82, v81
	v_fma_f32 v84, -v80, v83, v82
	v_fmac_f32_e32 v83, v84, v81
	v_fma_f32 v80, -v80, v83, v82
	v_div_fmas_f32 v80, v80, v81, v83
	v_pk_add_f32 v[82:83], v[76:77], -1.0 op_sel_hi:[1,0]
	v_div_fixup_f32 v80, v80, v71, v73
	v_pk_fma_f32 v[82:83], v[48:49], v[82:83], 1.0 op_sel_hi:[1,1,0]
	v_pk_mul_f32 v[76:77], v[80:81], v[76:77] op_sel_hi:[0,1]
	v_pk_mul_f32 v[82:83], v[82:83], v[72:73] op_sel_hi:[1,0]
	v_mov_b32_e32 v73, v1
	v_add_f32_e32 v71, v82, v83
	v_mul_f32_e32 v71, v74, v71
	v_mul_f32_e32 v72, v56, v71
	v_cvt_pk_bf16_f32 v74, v74, v75
	v_cvt_pk_bf16_f32 v75, v80, 0
	v_mov_b32_dpp v73, v72 quad_perm:[1,0,3,2] row_mask:0xf bank_mask:0xf
	v_fmac_f32_e32 v73, v56, v71
	v_cvt_pk_bf16_f32 v76, v76, v77
	v_cvt_pk_bf16_f32 v77, v82, v83
	v_add_f32_dpp v71, v73, v73 quad_perm:[2,3,0,1] row_mask:0xf bank_mask:0xf bound_ctrl:1
	v_lshl_add_u64 v[80:81], v[78:79], 4, s[52:53]
	s_nop 0
	v_add_f32_dpp v71, v71, v71 row_half_mirror row_mask:0xf bank_mask:0xf bound_ctrl:1
	s_nop 1
	v_add_f32_dpp v71, v71, v71 row_mirror row_mask:0xf bank_mask:0xf bound_ctrl:1
	v_mov_b32_e32 v72, v71
	s_nop 1
	v_permlane32_swap_b32 v71, v72
	global_store_dwordx4 v[80:81], v[74:77], off
	v_add_f32_e32 v71, v71, v72
	v_mov_b32_e32 v72, v71
	s_nop 1
	v_permlane16_swap_b32_e32 v71, v72
	v_lshl_add_u64 v[76:77], v[78:79], 1, s[58:59]
	global_store_short_d16_hi v[76:77], v74, off
	s_and_saveexec_b64 s[0:1], s[42:43]
	s_cbranch_execz .LBB0_425
	s_waitcnt lgkmcnt(0)
	v_add_f32_e32 v71, v71, v72
	v_mad_i64_i32 v[72:73], s[22:23], s22, 24, v[114:115]
	global_store_dword v[72:73], v71, off
.LBB0_425:
	s_or_b64 exec, exec, s[0:1]
	s_addk_i32 s21, 0xb00
	v_lshlrev_b32_e32 v74, 16, v69
	v_add_u32_e32 v69, s21, v58
	v_lshlrev_b32_e32 v75, 16, v70
	ds_read_u16 v70, v69 offset:3584
	ds_read_u16 v71, v69 offset:768
	s_waitcnt lgkmcnt(2)
	ds_read_u16 v72, v69 offset:6400
	ds_read_u16 v76, v69 offset:4352
	ds_read_u16 v78, v69 offset:5632
	ds_read_u16 v79, v69 offset:2816
	s_waitcnt lgkmcnt(5)
	v_lshlrev_b32_e32 v70, 16, v70
	s_waitcnt lgkmcnt(3)
	v_lshlrev_b32_e32 v73, 16, v72
	v_lshlrev_b32_e32 v72, 16, v71
	ds_read_u16 v77, v69 offset:1536
	ds_read_u16 v80, v69
	v_pk_add_f32 v[72:73], v[72:73], v[70:71] op_sel_hi:[1,0] neg_lo:[0,1] neg_hi:[0,1]
	ds_read_u16 v69, v69 offset:7168
	v_pk_mul_f32 v[72:73], v[54:55], v[72:73]
	s_waitcnt lgkmcnt(4)
	v_lshlrev_b32_e32 v78, 16, v78
	v_add_f32_e32 v70, v72, v70
	v_add_f32_e32 v70, v70, v73
	v_mul_f32_e32 v71, v0, v70
	s_waitcnt lgkmcnt(2)
	v_lshlrev_b32_e32 v73, 16, v77
	s_waitcnt lgkmcnt(1)
	v_lshlrev_b32_e32 v72, 16, v80
	v_mul_f32_e32 v77, v71, v71
	v_mov_b32_e32 v80, v1
	s_or_b32 s22, s20, s14
	s_nop 0
	v_mov_b32_dpp v80, v77 quad_perm:[1,0,3,2] row_mask:0xf bank_mask:0xf
	v_fmac_f32_e32 v80, v71, v71
	s_nop 1
	v_add_f32_dpp v77, v80, v80 quad_perm:[2,3,0,1] row_mask:0xf bank_mask:0xf bound_ctrl:1
	s_nop 1
	v_add_f32_dpp v77, v77, v77 row_half_mirror row_mask:0xf bank_mask:0xf bound_ctrl:1
	s_nop 1
	v_add_f32_dpp v77, v77, v77 row_mirror row_mask:0xf bank_mask:0xf bound_ctrl:1
	v_mov_b32_e32 v80, v77
	s_nop 1
	v_permlane32_swap_b32 v77, v80
	s_nop 0
	v_add_f32_e32 v80, v77, v80
	v_mov_b32_e32 v81, v80
	s_nop 1
	v_permlane16_swap_b32_e32 v80, v81
	v_lshlrev_b32_e32 v77, 16, v76
	v_lshlrev_b32_e32 v76, 16, v79
	s_waitcnt lgkmcnt(0)
	v_lshlrev_b32_e32 v79, 16, v69
	v_pk_add_f32 v[72:73], v[72:73], v[76:77] neg_lo:[0,1] neg_hi:[0,1]
	s_waitcnt lgkmcnt(0)
	v_add_f32_e32 v69, v80, v81
	v_mul_f32_e32 v80, 0x4f800000, v69
	v_cmp_gt_f32_e32 vcc, s45, v69
	v_pk_fma_f32 v[72:73], v[50:51], v[72:73], v[76:77]
	v_pk_add_f32 v[76:77], v[78:79], v[76:77] neg_lo:[0,1] neg_hi:[0,1]
	v_cndmask_b32_e32 v69, v69, v80, vcc
	v_sqrt_f32_e32 v80, v69
	v_pk_fma_f32 v[72:73], v[52:53], v[76:77], v[72:73]
	v_add_u32_e32 v78, -1, v80
	v_fma_f32 v79, -v78, v80, v69
	v_cmp_ge_f32_e64 s[0:1], 0, v79
	v_add_u32_e32 v79, 1, v80
	s_nop 0
	v_cndmask_b32_e64 v78, v80, v78, s[0:1]
	v_fma_f32 v80, -v79, v80, v69
	v_cmp_lt_f32_e64 s[0:1], 0, v80
	s_nop 1
	v_cndmask_b32_e64 v78, v78, v79, s[0:1]
	v_mul_f32_e32 v79, 0x37800000, v78
	v_cndmask_b32_e32 v78, v78, v79, vcc
	v_cmp_class_f32_e32 vcc, v69, v207
	v_mad_i64_i32 v[76:77], s[0:1], s22, v214, v[46:47]
	s_nop 0
	v_cndmask_b32_e32 v69, v78, v69, vcc
	v_max_f32_e32 v69, 0x2b8cbccc, v69
	v_div_scale_f32 v78, s[0:1], v69, v69, v71
	v_rcp_f32_e32 v79, v78
	s_nop 0
	v_fma_f32 v80, -v78, v79, 1.0
	v_fmac_f32_e32 v79, v80, v79
	v_div_scale_f32 v80, vcc, v71, v69, v71
	v_mul_f32_e32 v81, v80, v79
	v_fma_f32 v82, -v78, v81, v80
	v_fmac_f32_e32 v81, v82, v79
	v_fma_f32 v78, -v78, v81, v80
	v_div_fmas_f32 v78, v78, v79, v81
	v_pk_add_f32 v[80:81], v[74:75], -1.0 op_sel_hi:[1,0]
	v_div_fixup_f32 v78, v78, v69, v71
	v_pk_fma_f32 v[80:81], v[48:49], v[80:81], 1.0 op_sel_hi:[1,1,0]
	v_pk_mul_f32 v[74:75], v[78:79], v[74:75] op_sel_hi:[0,1]
	v_pk_mul_f32 v[80:81], v[80:81], v[70:71] op_sel_hi:[1,0]
	v_mov_b32_e32 v71, v1
	v_add_f32_e32 v69, v80, v81
	v_mul_f32_e32 v69, v72, v69
	v_mul_f32_e32 v70, v56, v69
	v_cvt_pk_bf16_f32 v72, v72, v73
	v_cvt_pk_bf16_f32 v73, v78, 0
	v_mov_b32_dpp v71, v70 quad_perm:[1,0,3,2] row_mask:0xf bank_mask:0xf
	v_fmac_f32_e32 v71, v56, v69
	v_cvt_pk_bf16_f32 v74, v74, v75
	v_cvt_pk_bf16_f32 v75, v80, v81
	v_add_f32_dpp v69, v71, v71 quad_perm:[2,3,0,1] row_mask:0xf bank_mask:0xf bound_ctrl:1
	v_lshl_add_u64 v[78:79], v[76:77], 4, s[52:53]
	s_nop 0
	v_add_f32_dpp v69, v69, v69 row_half_mirror row_mask:0xf bank_mask:0xf bound_ctrl:1
	s_nop 1
	v_add_f32_dpp v69, v69, v69 row_mirror row_mask:0xf bank_mask:0xf bound_ctrl:1
	v_mov_b32_e32 v70, v69
	s_nop 1
	v_permlane32_swap_b32 v69, v70
	global_store_dwordx4 v[78:79], v[72:75], off
	v_add_f32_e32 v69, v69, v70
	v_mov_b32_e32 v70, v69
	s_nop 1
	v_permlane16_swap_b32_e32 v69, v70
	v_lshl_add_u64 v[74:75], v[76:77], 1, s[58:59]
	global_store_short_d16_hi v[74:75], v72, off
	s_and_saveexec_b64 s[0:1], s[42:43]
	s_cbranch_execz .LBB0_427
	s_waitcnt lgkmcnt(0)
	v_add_f32_e32 v69, v69, v70
	v_mad_i64_i32 v[70:71], s[22:23], s22, 24, v[114:115]
	global_store_dword v[70:71], v69, off
.LBB0_427:
	s_or_b64 exec, exec, s[0:1]
	s_addk_i32 s21, 0xb00
	v_lshlrev_b32_e32 v72, 16, v67
	v_add_u32_e32 v67, s21, v58
	v_lshlrev_b32_e32 v73, 16, v68
	ds_read_u16 v68, v67 offset:3584
	ds_read_u16 v69, v67 offset:768
	s_waitcnt lgkmcnt(2)
	ds_read_u16 v70, v67 offset:6400
	ds_read_u16 v74, v67 offset:4352
	ds_read_u16 v76, v67 offset:5632
	ds_read_u16 v77, v67 offset:2816
	s_waitcnt lgkmcnt(5)
	v_lshlrev_b32_e32 v68, 16, v68
	s_waitcnt lgkmcnt(3)
	v_lshlrev_b32_e32 v71, 16, v70
	ds_read_u16 v75, v67 offset:1536
	ds_read_u16 v78, v67
	v_lshlrev_b32_e32 v70, 16, v69
	v_pk_add_f32 v[70:71], v[70:71], v[68:69] op_sel_hi:[1,0] neg_lo:[0,1] neg_hi:[0,1]
	v_mov_b32_e32 v79, v1
	v_pk_mul_f32 v[70:71], v[54:55], v[70:71]
	ds_read_u16 v69, v67 offset:7168
	v_add_f32_e32 v68, v70, v68
	v_add_f32_e32 v68, v68, v71
	s_waitcnt lgkmcnt(1)
	v_lshlrev_b32_e32 v70, 16, v78
	v_mul_f32_e32 v78, v0, v68
	v_lshlrev_b32_e32 v71, 16, v75
	v_mul_f32_e32 v75, v78, v78
	v_lshlrev_b32_e32 v76, 16, v76
	s_or_b32 s22, s20, s15
	v_mov_b32_dpp v79, v75 quad_perm:[1,0,3,2] row_mask:0xf bank_mask:0xf
	v_fmac_f32_e32 v79, v78, v78
	s_nop 1
	v_add_f32_dpp v75, v79, v79 quad_perm:[2,3,0,1] row_mask:0xf bank_mask:0xf bound_ctrl:1
	s_nop 1
	v_add_f32_dpp v75, v75, v75 row_half_mirror row_mask:0xf bank_mask:0xf bound_ctrl:1
	s_nop 1
	v_add_f32_dpp v75, v75, v75 row_mirror row_mask:0xf bank_mask:0xf bound_ctrl:1
	v_mov_b32_e32 v79, v75
	s_nop 1
	v_permlane32_swap_b32 v79, v75
	s_nop 0
	v_add_f32_e32 v79, v79, v75
	v_mov_b32_e32 v80, v79
	s_nop 1
	v_permlane16_swap_b32_e32 v79, v80
	v_lshlrev_b32_e32 v75, 16, v74
	v_lshlrev_b32_e32 v74, 16, v77
	s_waitcnt lgkmcnt(0)
	v_lshlrev_b32_e32 v77, 16, v69
	v_pk_add_f32 v[70:71], v[70:71], v[74:75] neg_lo:[0,1] neg_hi:[0,1]
	s_waitcnt lgkmcnt(0)
	v_add_f32_e32 v69, v79, v80
	v_mul_f32_e32 v79, 0x4f800000, v69
	v_cmp_gt_f32_e32 vcc, s45, v69
	v_pk_fma_f32 v[70:71], v[50:51], v[70:71], v[74:75]
	v_pk_add_f32 v[74:75], v[76:77], v[74:75] neg_lo:[0,1] neg_hi:[0,1]
	v_cndmask_b32_e32 v69, v69, v79, vcc
	v_sqrt_f32_e32 v79, v69
	v_pk_fma_f32 v[70:71], v[52:53], v[74:75], v[70:71]
	v_add_u32_e32 v76, -1, v79
	v_fma_f32 v77, -v76, v79, v69
	v_cmp_ge_f32_e64 s[0:1], 0, v77
	v_add_u32_e32 v77, 1, v79
	s_nop 0
	v_cndmask_b32_e64 v76, v79, v76, s[0:1]
	v_fma_f32 v79, -v77, v79, v69
	v_cmp_lt_f32_e64 s[0:1], 0, v79
	s_nop 1
	v_cndmask_b32_e64 v76, v76, v77, s[0:1]
	v_mul_f32_e32 v77, 0x37800000, v76
	v_cndmask_b32_e32 v76, v76, v77, vcc
	v_cmp_class_f32_e32 vcc, v69, v207
	v_mad_i64_i32 v[74:75], s[0:1], s22, v214, v[46:47]
	s_nop 0
	v_cndmask_b32_e32 v69, v76, v69, vcc
	v_max_f32_e32 v69, 0x2b8cbccc, v69
	v_div_scale_f32 v76, s[0:1], v69, v69, v78
	v_rcp_f32_e32 v77, v76
	s_nop 0
	v_fma_f32 v79, -v76, v77, 1.0
	v_fmac_f32_e32 v77, v79, v77
	v_div_scale_f32 v79, vcc, v78, v69, v78
	v_mul_f32_e32 v80, v79, v77
	v_fma_f32 v81, -v76, v80, v79
	v_fmac_f32_e32 v80, v81, v77
	v_fma_f32 v76, -v76, v80, v79
	v_div_fmas_f32 v76, v76, v77, v80
	v_div_fixup_f32 v76, v76, v69, v78
	v_pk_add_f32 v[78:79], v[72:73], -1.0 op_sel_hi:[1,0]
	v_mov_b32_e32 v77, v1
	v_pk_fma_f32 v[78:79], v[48:49], v[78:79], 1.0 op_sel_hi:[1,1,0]
	s_nop 0
	v_pk_mul_f32 v[78:79], v[78:79], v[68:69] op_sel_hi:[1,0]
	s_nop 0
	v_add_f32_e32 v68, v78, v79
	v_mul_f32_e32 v68, v70, v68
	v_mul_f32_e32 v69, v56, v68
	v_cvt_pk_bf16_f32 v70, v70, v71
	v_cvt_pk_bf16_f32 v71, v76, 0
	v_mov_b32_dpp v77, v69 quad_perm:[1,0,3,2] row_mask:0xf bank_mask:0xf
	v_fmac_f32_e32 v77, v56, v68
	v_pk_mul_f32 v[72:73], v[76:77], v[72:73] op_sel_hi:[0,1]
	v_cvt_pk_bf16_f32 v72, v72, v73
	v_add_f32_dpp v68, v77, v77 quad_perm:[2,3,0,1] row_mask:0xf bank_mask:0xf bound_ctrl:1
	v_cvt_pk_bf16_f32 v73, v78, v79
	v_lshl_add_u64 v[76:77], v[74:75], 4, s[52:53]
	v_add_f32_dpp v68, v68, v68 row_half_mirror row_mask:0xf bank_mask:0xf bound_ctrl:1
	s_nop 1
	v_add_f32_dpp v68, v68, v68 row_mirror row_mask:0xf bank_mask:0xf bound_ctrl:1
	v_mov_b32_e32 v69, v68
	s_nop 1
	v_permlane32_swap_b32 v69, v68
	global_store_dwordx4 v[76:77], v[70:73], off
	v_add_f32_e32 v68, v69, v68
	v_mov_b32_e32 v69, v68
	s_nop 1
	v_permlane16_swap_b32_e32 v68, v69
	v_lshl_add_u64 v[72:73], v[74:75], 1, s[58:59]
	global_store_short_d16_hi v[72:73], v70, off
	s_and_saveexec_b64 s[0:1], s[42:43]
	s_cbranch_execz .LBB0_429
	s_waitcnt lgkmcnt(0)
	v_add_f32_e32 v70, v68, v69
	v_mad_i64_i32 v[68:69], s[22:23], s22, 24, v[114:115]
	global_store_dword v[68:69], v70, off
.LBB0_429:
	s_or_b64 exec, exec, s[0:1]
	v_lshlrev_b32_e32 v70, 16, v65
	ds_read_u16 v65, v67 offset:6400
	ds_read_u16 v68, v67 offset:3584
	s_waitcnt lgkmcnt(2)
	ds_read_u16 v69, v67 offset:9216
	ds_read_u16 v72, v67 offset:7168
	ds_read_u16 v74, v67 offset:8448
	ds_read_u16 v75, v67 offset:5632
	v_lshlrev_b32_e32 v71, 16, v66
	s_waitcnt lgkmcnt(5)
	v_lshlrev_b32_e32 v66, 16, v65
	s_waitcnt lgkmcnt(3)
	v_lshlrev_b32_e32 v69, 16, v69
	v_lshlrev_b32_e32 v68, 16, v68
	ds_read_u16 v65, v67 offset:4352
	ds_read_u16 v73, v67 offset:2816
	v_pk_add_f32 v[68:69], v[68:69], v[66:67] op_sel_hi:[1,0] neg_lo:[0,1] neg_hi:[0,1]
	v_mov_b32_e32 v77, v1
	v_pk_mul_f32 v[68:69], v[54:55], v[68:69]
	s_waitcnt lgkmcnt(3)
	v_lshlrev_b32_e32 v74, 16, v74
	v_add_f32_e32 v66, v68, v66
	v_add_f32_e32 v66, v66, v69
	v_mul_f32_e32 v76, v0, v66
	s_waitcnt lgkmcnt(0)
	v_lshlrev_b32_e32 v68, 16, v73
	v_mul_f32_e32 v73, v76, v76
	v_lshlrev_b32_e32 v69, 16, v65
	ds_read_u16 v65, v67 offset:9984
	v_mov_b32_dpp v77, v73 quad_perm:[1,0,3,2] row_mask:0xf bank_mask:0xf
	v_fmac_f32_e32 v77, v76, v76
	s_or_b32 s21, s20, s16
	s_nop 0
	v_add_f32_dpp v73, v77, v77 quad_perm:[2,3,0,1] row_mask:0xf bank_mask:0xf bound_ctrl:1
	s_nop 1
	v_add_f32_dpp v73, v73, v73 row_half_mirror row_mask:0xf bank_mask:0xf bound_ctrl:1
	s_nop 1
	v_add_f32_dpp v73, v73, v73 row_mirror row_mask:0xf bank_mask:0xf bound_ctrl:1
	v_mov_b32_e32 v77, v73
	s_nop 1
	v_permlane32_swap_b32 v73, v77
	s_nop 0
	v_add_f32_e32 v77, v73, v77
	v_mov_b32_e32 v78, v77
	s_nop 1
	v_permlane16_swap_b32_e32 v77, v78
	v_lshlrev_b32_e32 v73, 16, v72
	v_lshlrev_b32_e32 v72, 16, v75
	s_waitcnt lgkmcnt(0)
	v_lshlrev_b32_e32 v75, 16, v65
	v_pk_add_f32 v[68:69], v[68:69], v[72:73] neg_lo:[0,1] neg_hi:[0,1]
	s_waitcnt lgkmcnt(0)
	v_add_f32_e32 v65, v77, v78
	v_mul_f32_e32 v77, 0x4f800000, v65
	v_cmp_gt_f32_e32 vcc, s45, v65
	v_pk_fma_f32 v[68:69], v[50:51], v[68:69], v[72:73]
	v_pk_add_f32 v[72:73], v[74:75], v[72:73] neg_lo:[0,1] neg_hi:[0,1]
	v_cndmask_b32_e32 v65, v65, v77, vcc
	v_sqrt_f32_e32 v77, v65
	v_pk_fma_f32 v[68:69], v[52:53], v[72:73], v[68:69]
	v_add_u32_e32 v74, -1, v77
	v_fma_f32 v75, -v74, v77, v65
	v_cmp_ge_f32_e64 s[0:1], 0, v75
	v_add_u32_e32 v75, 1, v77
	s_nop 0
	v_cndmask_b32_e64 v74, v77, v74, s[0:1]
	v_fma_f32 v77, -v75, v77, v65
	v_cmp_lt_f32_e64 s[0:1], 0, v77
	s_nop 1
	v_cndmask_b32_e64 v74, v74, v75, s[0:1]
	v_mul_f32_e32 v75, 0x37800000, v74
	v_cndmask_b32_e32 v74, v74, v75, vcc
	v_cmp_class_f32_e32 vcc, v65, v207
	v_mad_i64_i32 v[72:73], s[0:1], s21, v214, v[46:47]
	s_nop 0
	v_cndmask_b32_e32 v65, v74, v65, vcc
	v_max_f32_e32 v65, 0x2b8cbccc, v65
	v_div_scale_f32 v74, s[0:1], v65, v65, v76
	v_rcp_f32_e32 v75, v74
	s_nop 0
	v_fma_f32 v77, -v74, v75, 1.0
	v_fmac_f32_e32 v75, v77, v75
	v_div_scale_f32 v77, vcc, v76, v65, v76
	v_mul_f32_e32 v78, v77, v75
	v_fma_f32 v79, -v74, v78, v77
	v_fmac_f32_e32 v78, v79, v75
	v_fma_f32 v74, -v74, v78, v77
	v_div_fmas_f32 v74, v74, v75, v78
	v_div_fixup_f32 v74, v74, v65, v76
	v_pk_add_f32 v[76:77], v[70:71], -1.0 op_sel_hi:[1,0]
	v_mov_b32_e32 v75, v1
	v_pk_fma_f32 v[76:77], v[48:49], v[76:77], 1.0 op_sel_hi:[1,1,0]
	s_nop 0
	v_pk_mul_f32 v[76:77], v[76:77], v[66:67] op_sel_hi:[1,0]
	s_nop 0
	v_add_f32_e32 v65, v76, v77
	v_mul_f32_e32 v65, v68, v65
	v_mul_f32_e32 v66, v56, v65
	v_cvt_pk_bf16_f32 v68, v68, v69
	v_cvt_pk_bf16_f32 v69, v74, 0
	v_mov_b32_dpp v75, v66 quad_perm:[1,0,3,2] row_mask:0xf bank_mask:0xf
	v_fmac_f32_e32 v75, v56, v65
	v_pk_mul_f32 v[70:71], v[74:75], v[70:71] op_sel_hi:[0,1]
	v_cvt_pk_bf16_f32 v70, v70, v71
	v_add_f32_dpp v65, v75, v75 quad_perm:[2,3,0,1] row_mask:0xf bank_mask:0xf bound_ctrl:1
	v_cvt_pk_bf16_f32 v71, v76, v77
	v_lshl_add_u64 v[74:75], v[72:73], 4, s[52:53]
	v_add_f32_dpp v65, v65, v65 row_half_mirror row_mask:0xf bank_mask:0xf bound_ctrl:1
	s_nop 1
	v_add_f32_dpp v65, v65, v65 row_mirror row_mask:0xf bank_mask:0xf bound_ctrl:1
	v_mov_b32_e32 v66, v65
	s_nop 1
	v_permlane32_swap_b32 v65, v66
	global_store_dwordx4 v[74:75], v[68:71], off
	v_add_f32_e32 v65, v65, v66
	v_mov_b32_e32 v66, v65
	s_nop 1
	v_permlane16_swap_b32_e32 v65, v66
	v_lshl_add_u64 v[70:71], v[72:73], 1, s[58:59]
	global_store_short_d16_hi v[70:71], v68, off
	s_and_saveexec_b64 s[0:1], s[42:43]
	s_cbranch_execz .LBB0_431
	s_waitcnt lgkmcnt(0)
	v_add_f32_e32 v65, v65, v66
	v_mad_i64_i32 v[68:69], s[22:23], s21, 24, v[114:115]
	global_store_dword v[68:69], v65, off
.LBB0_431:
	s_or_b64 exec, exec, s[0:1]
	v_lshlrev_b32_e32 v70, 16, v63
	ds_read_u16 v63, v67 offset:9216
	ds_read_u16 v65, v67 offset:6400
	s_waitcnt lgkmcnt(2)
	ds_read_u16 v66, v67 offset:12032
	ds_read_u16 v72, v67 offset:9984
	ds_read_u16 v74, v67 offset:11264
	ds_read_u16 v75, v67 offset:8448
	v_lshlrev_b32_e32 v71, 16, v64
	s_waitcnt lgkmcnt(5)
	v_lshlrev_b32_e32 v64, 16, v63
	s_waitcnt lgkmcnt(3)
	v_lshlrev_b32_e32 v69, 16, v66
	v_lshlrev_b32_e32 v68, 16, v65
	ds_read_u16 v63, v67 offset:7168
	ds_read_u16 v66, v67 offset:5632
	v_pk_add_f32 v[68:69], v[68:69], v[64:65] op_sel_hi:[1,0] neg_lo:[0,1] neg_hi:[0,1]
	v_mov_b32_e32 v73, v1
	v_pk_mul_f32 v[68:69], v[54:55], v[68:69]
	s_waitcnt lgkmcnt(3)
	v_lshlrev_b32_e32 v74, 16, v74
	v_add_f32_e32 v64, v68, v64
	v_add_f32_e32 v64, v64, v69
	v_mul_f32_e32 v65, v0, v64
	s_waitcnt lgkmcnt(0)
	v_lshlrev_b32_e32 v68, 16, v66
	v_mul_f32_e32 v66, v65, v65
	v_lshlrev_b32_e32 v69, 16, v63
	ds_read_u16 v63, v67 offset:12800
	v_mov_b32_dpp v73, v66 quad_perm:[1,0,3,2] row_mask:0xf bank_mask:0xf
	v_fmac_f32_e32 v73, v65, v65
	s_or_b32 s21, s20, s17
	s_nop 0
	v_add_f32_dpp v66, v73, v73 quad_perm:[2,3,0,1] row_mask:0xf bank_mask:0xf bound_ctrl:1
	s_nop 1
	v_add_f32_dpp v66, v66, v66 row_half_mirror row_mask:0xf bank_mask:0xf bound_ctrl:1
	s_nop 1
	v_add_f32_dpp v66, v66, v66 row_mirror row_mask:0xf bank_mask:0xf bound_ctrl:1
	v_mov_b32_e32 v73, v66
	s_nop 1
	v_permlane32_swap_b32 v66, v73
	s_nop 0
	v_add_f32_e32 v66, v66, v73
	v_mov_b32_e32 v76, v66
	s_nop 1
	v_permlane16_swap_b32_e32 v66, v76
	v_lshlrev_b32_e32 v73, 16, v72
	v_lshlrev_b32_e32 v72, 16, v75
	s_waitcnt lgkmcnt(0)
	v_lshlrev_b32_e32 v75, 16, v63
	v_pk_add_f32 v[68:69], v[68:69], v[72:73] neg_lo:[0,1] neg_hi:[0,1]
	s_waitcnt lgkmcnt(0)
	v_add_f32_e32 v63, v66, v76
	v_mul_f32_e32 v66, 0x4f800000, v63
	v_cmp_gt_f32_e32 vcc, s45, v63
	v_pk_fma_f32 v[68:69], v[50:51], v[68:69], v[72:73]
	v_pk_add_f32 v[72:73], v[74:75], v[72:73] neg_lo:[0,1] neg_hi:[0,1]
	v_cndmask_b32_e32 v63, v63, v66, vcc
	v_sqrt_f32_e32 v66, v63
	v_pk_fma_f32 v[68:69], v[52:53], v[72:73], v[68:69]
	v_add_u32_e32 v74, -1, v66
	v_fma_f32 v75, -v74, v66, v63
	v_cmp_ge_f32_e64 s[0:1], 0, v75
	v_add_u32_e32 v75, 1, v66
	s_nop 0
	v_cndmask_b32_e64 v74, v66, v74, s[0:1]
	v_fma_f32 v66, -v75, v66, v63
	v_cmp_lt_f32_e64 s[0:1], 0, v66
	s_nop 1
	v_cndmask_b32_e64 v66, v74, v75, s[0:1]
	v_mul_f32_e32 v74, 0x37800000, v66
	v_cndmask_b32_e32 v66, v66, v74, vcc
	v_cmp_class_f32_e32 vcc, v63, v207
	v_mad_i64_i32 v[72:73], s[0:1], s21, v214, v[46:47]
	s_nop 0
	v_cndmask_b32_e32 v63, v66, v63, vcc
	v_max_f32_e32 v63, 0x2b8cbccc, v63
	v_div_scale_f32 v66, s[0:1], v63, v63, v65
	v_rcp_f32_e32 v74, v66
	s_nop 0
	v_fma_f32 v75, -v66, v74, 1.0
	v_fmac_f32_e32 v74, v75, v74
	v_div_scale_f32 v75, vcc, v65, v63, v65
	v_mul_f32_e32 v76, v75, v74
	v_fma_f32 v77, -v66, v76, v75
	v_fmac_f32_e32 v76, v77, v74
	v_fma_f32 v66, -v66, v76, v75
	v_div_fmas_f32 v66, v66, v74, v76
	v_pk_add_f32 v[74:75], v[70:71], -1.0 op_sel_hi:[1,0]
	v_div_fixup_f32 v66, v66, v63, v65
	v_pk_fma_f32 v[74:75], v[48:49], v[74:75], 1.0 op_sel_hi:[1,1,0]
	v_pk_mul_f32 v[70:71], v[66:67], v[70:71] op_sel_hi:[0,1]
	v_pk_mul_f32 v[74:75], v[74:75], v[64:65] op_sel_hi:[1,0]
	v_mov_b32_e32 v65, v1
	v_add_f32_e32 v63, v74, v75
	v_mul_f32_e32 v63, v68, v63
	v_mul_f32_e32 v64, v56, v63
	v_cvt_pk_bf16_f32 v68, v68, v69
	v_cvt_pk_bf16_f32 v69, v66, 0
	v_mov_b32_dpp v65, v64 quad_perm:[1,0,3,2] row_mask:0xf bank_mask:0xf
	v_fmac_f32_e32 v65, v56, v63
	v_cvt_pk_bf16_f32 v70, v70, v71
	v_cvt_pk_bf16_f32 v71, v74, v75
	v_add_f32_dpp v63, v65, v65 quad_perm:[2,3,0,1] row_mask:0xf bank_mask:0xf bound_ctrl:1
	v_lshl_add_u64 v[74:75], v[72:73], 4, s[52:53]
	s_nop 0
	v_add_f32_dpp v63, v63, v63 row_half_mirror row_mask:0xf bank_mask:0xf bound_ctrl:1
	s_nop 1
	v_add_f32_dpp v63, v63, v63 row_mirror row_mask:0xf bank_mask:0xf bound_ctrl:1
	v_mov_b32_e32 v64, v63
	s_nop 1
	v_permlane32_swap_b32 v63, v64
	global_store_dwordx4 v[74:75], v[68:71], off
	v_add_f32_e32 v63, v63, v64
	v_mov_b32_e32 v64, v63
	s_nop 1
	v_permlane16_swap_b32_e32 v63, v64
	v_lshl_add_u64 v[70:71], v[72:73], 1, s[58:59]
	global_store_short_d16_hi v[70:71], v68, off
	s_and_saveexec_b64 s[0:1], s[42:43]
	s_cbranch_execz .LBB0_433
	s_waitcnt lgkmcnt(0)
	v_add_f32_e32 v63, v63, v64
	v_mad_i64_i32 v[64:65], s[22:23], s21, 24, v[114:115]
	global_store_dword v[64:65], v63, off
.LBB0_433:
	s_or_b64 exec, exec, s[0:1]
	s_waitcnt lgkmcnt(0)
	v_lshlrev_b32_e32 v64, 16, v61
	ds_read_u16 v61, v67 offset:12032
	ds_read_u16 v63, v67 offset:9216
	ds_read_u16 v66, v67 offset:14848
	ds_read_u16 v70, v67 offset:12800
	ds_read_u16 v72, v67 offset:14080
	ds_read_u16 v73, v67 offset:11264
	v_lshlrev_b32_e32 v65, 16, v62
	s_waitcnt lgkmcnt(5)
	v_lshlrev_b32_e32 v62, 16, v61
	s_waitcnt lgkmcnt(3)
	v_lshlrev_b32_e32 v69, 16, v66
	v_lshlrev_b32_e32 v68, 16, v63
	ds_read_u16 v61, v67 offset:9984
	ds_read_u16 v66, v67 offset:8448
	v_pk_add_f32 v[68:69], v[68:69], v[62:63] op_sel_hi:[1,0] neg_lo:[0,1] neg_hi:[0,1]
	v_mov_b32_e32 v71, v1
	v_pk_mul_f32 v[68:69], v[54:55], v[68:69]
	s_waitcnt lgkmcnt(3)
	v_lshlrev_b32_e32 v72, 16, v72
	v_add_f32_e32 v62, v68, v62
	v_add_f32_e32 v62, v62, v69
	v_mul_f32_e32 v63, v0, v62
	s_waitcnt lgkmcnt(0)
	v_lshlrev_b32_e32 v68, 16, v66
	v_mul_f32_e32 v66, v63, v63
	v_lshlrev_b32_e32 v69, 16, v61
	ds_read_u16 v61, v67 offset:15616
	v_mov_b32_dpp v71, v66 quad_perm:[1,0,3,2] row_mask:0xf bank_mask:0xf
	v_fmac_f32_e32 v71, v63, v63
	s_or_b32 s21, s20, s18
	s_nop 0
	v_add_f32_dpp v66, v71, v71 quad_perm:[2,3,0,1] row_mask:0xf bank_mask:0xf bound_ctrl:1
	s_nop 1
	v_add_f32_dpp v66, v66, v66 row_half_mirror row_mask:0xf bank_mask:0xf bound_ctrl:1
	s_nop 1
	v_add_f32_dpp v66, v66, v66 row_mirror row_mask:0xf bank_mask:0xf bound_ctrl:1
	v_mov_b32_e32 v71, v66
	s_nop 1
	v_permlane32_swap_b32 v66, v71
	s_nop 0
	v_add_f32_e32 v66, v66, v71
	v_mov_b32_e32 v74, v66
	s_nop 1
	v_permlane16_swap_b32_e32 v66, v74
	v_lshlrev_b32_e32 v71, 16, v70
	v_lshlrev_b32_e32 v70, 16, v73
	s_waitcnt lgkmcnt(0)
	v_lshlrev_b32_e32 v73, 16, v61
	v_pk_add_f32 v[68:69], v[68:69], v[70:71] neg_lo:[0,1] neg_hi:[0,1]
	s_waitcnt lgkmcnt(0)
	v_add_f32_e32 v61, v66, v74
	v_mul_f32_e32 v66, 0x4f800000, v61
	v_cmp_gt_f32_e32 vcc, s45, v61
	v_pk_fma_f32 v[68:69], v[50:51], v[68:69], v[70:71]
	v_pk_add_f32 v[70:71], v[72:73], v[70:71] neg_lo:[0,1] neg_hi:[0,1]
	v_cndmask_b32_e32 v61, v61, v66, vcc
	v_sqrt_f32_e32 v66, v61
	v_pk_fma_f32 v[68:69], v[52:53], v[70:71], v[68:69]
	v_add_u32_e32 v72, -1, v66
	v_fma_f32 v73, -v72, v66, v61
	v_cmp_ge_f32_e64 s[0:1], 0, v73
	v_add_u32_e32 v73, 1, v66
	s_nop 0
	v_cndmask_b32_e64 v72, v66, v72, s[0:1]
	v_fma_f32 v66, -v73, v66, v61
	v_cmp_lt_f32_e64 s[0:1], 0, v66
	s_nop 1
	v_cndmask_b32_e64 v66, v72, v73, s[0:1]
	v_mul_f32_e32 v72, 0x37800000, v66
	v_cndmask_b32_e32 v66, v66, v72, vcc
	v_cmp_class_f32_e32 vcc, v61, v207
	v_mad_i64_i32 v[72:73], s[0:1], s21, v214, v[46:47]
	s_nop 0
	v_cndmask_b32_e32 v61, v66, v61, vcc
	v_max_f32_e32 v61, 0x2b8cbccc, v61
	v_div_scale_f32 v66, s[0:1], v61, v61, v63
	v_rcp_f32_e32 v74, v66
	s_nop 0
	v_fma_f32 v70, -v66, v74, 1.0
	v_fmac_f32_e32 v74, v70, v74
	v_div_scale_f32 v70, vcc, v63, v61, v63
	v_mul_f32_e32 v71, v70, v74
	v_fma_f32 v75, -v66, v71, v70
	v_fmac_f32_e32 v71, v75, v74
	v_fma_f32 v66, -v66, v71, v70
	v_div_fmas_f32 v66, v66, v74, v71
	v_pk_add_f32 v[70:71], v[64:65], -1.0 op_sel_hi:[1,0]
	v_div_fixup_f32 v66, v66, v61, v63
	v_pk_fma_f32 v[70:71], v[48:49], v[70:71], 1.0 op_sel_hi:[1,1,0]
	v_pk_mul_f32 v[64:65], v[66:67], v[64:65] op_sel_hi:[0,1]
	v_pk_mul_f32 v[74:75], v[70:71], v[62:63] op_sel_hi:[1,0]
	v_mov_b32_e32 v63, v1
	v_add_f32_e32 v61, v74, v75
	v_mul_f32_e32 v61, v68, v61
	v_mul_f32_e32 v62, v56, v61
	v_cvt_pk_bf16_f32 v68, v68, v69
	v_cvt_pk_bf16_f32 v69, v66, 0
	v_mov_b32_dpp v63, v62 quad_perm:[1,0,3,2] row_mask:0xf bank_mask:0xf
	v_fmac_f32_e32 v63, v56, v61
	v_cvt_pk_bf16_f32 v70, v64, v65
	v_cvt_pk_bf16_f32 v71, v74, v75
	v_add_f32_dpp v61, v63, v63 quad_perm:[2,3,0,1] row_mask:0xf bank_mask:0xf bound_ctrl:1
	v_lshl_add_u64 v[64:65], v[72:73], 4, s[52:53]
	s_nop 0
	v_add_f32_dpp v61, v61, v61 row_half_mirror row_mask:0xf bank_mask:0xf bound_ctrl:1
	s_nop 1
	v_add_f32_dpp v61, v61, v61 row_mirror row_mask:0xf bank_mask:0xf bound_ctrl:1
	v_mov_b32_e32 v62, v61
	s_nop 1
	v_permlane32_swap_b32 v61, v62
	global_store_dwordx4 v[64:65], v[68:71], off
	v_add_f32_e32 v61, v61, v62
	v_mov_b32_e32 v62, v61
	s_nop 1
	v_permlane16_swap_b32_e32 v61, v62
	v_lshl_add_u64 v[64:65], v[72:73], 1, s[58:59]
	global_store_short_d16_hi v[64:65], v68, off
	s_and_saveexec_b64 s[0:1], s[42:43]
	s_cbranch_execz .LBB0_435
	s_waitcnt lgkmcnt(0)
	v_add_f32_e32 v61, v61, v62
	v_mad_i64_i32 v[62:63], s[22:23], s21, 24, v[114:115]
	global_store_dword v[62:63], v61, off
.LBB0_435:
	s_or_b64 exec, exec, s[0:1]
	v_lshlrev_b32_e32 v64, 16, v59
	ds_read_u16 v59, v67 offset:14848
	ds_read_u16 v61, v67 offset:12032
	s_waitcnt lgkmcnt(2)
	ds_read_u16 v62, v67 offset:17664
	ds_read_u16 v66, v67 offset:15616
	ds_read_u16 v68, v67 offset:16896
	ds_read_u16 v69, v67 offset:14080
	v_lshlrev_b32_e32 v65, 16, v60
	s_waitcnt lgkmcnt(5)
	v_lshlrev_b32_e32 v60, 16, v59
	s_waitcnt lgkmcnt(3)
	v_lshlrev_b32_e32 v63, 16, v62
	v_lshlrev_b32_e32 v62, 16, v61
	ds_read_u16 v59, v67 offset:12800
	ds_read_u16 v70, v67 offset:11264
	v_pk_add_f32 v[62:63], v[62:63], v[60:61] op_sel_hi:[1,0] neg_lo:[0,1] neg_hi:[0,1]
	s_waitcnt lgkmcnt(3)
	v_lshlrev_b32_e32 v68, 16, v68
	v_pk_mul_f32 v[62:63], v[54:55], v[62:63]
	s_or_b32 s20, s20, s19
	v_add_f32_e32 v60, v62, v60
	v_add_f32_e32 v60, v60, v63
	v_mul_f32_e32 v61, v0, v60
	s_waitcnt lgkmcnt(1)
	v_lshlrev_b32_e32 v63, 16, v59
	s_waitcnt lgkmcnt(0)
	v_lshlrev_b32_e32 v62, 16, v70
	ds_read_u16 v59, v67 offset:18432
	v_mul_f32_e32 v67, v61, v61
	v_mov_b32_e32 v70, v1
	s_nop 1
	v_mov_b32_dpp v70, v67 quad_perm:[1,0,3,2] row_mask:0xf bank_mask:0xf
	v_fmac_f32_e32 v70, v61, v61
	s_nop 1
	v_add_f32_dpp v67, v70, v70 quad_perm:[2,3,0,1] row_mask:0xf bank_mask:0xf bound_ctrl:1
	s_nop 1
	v_add_f32_dpp v67, v67, v67 row_half_mirror row_mask:0xf bank_mask:0xf bound_ctrl:1
	s_nop 1
	v_add_f32_dpp v67, v67, v67 row_mirror row_mask:0xf bank_mask:0xf bound_ctrl:1
	v_mov_b32_e32 v70, v67
	s_nop 1
	v_permlane32_swap_b32 v67, v70
	s_nop 0
	v_add_f32_e32 v70, v67, v70
	v_mov_b32_e32 v71, v70
	s_nop 1
	v_permlane16_swap_b32_e32 v70, v71
	v_lshlrev_b32_e32 v67, 16, v66
	v_lshlrev_b32_e32 v66, 16, v69
	s_waitcnt lgkmcnt(0)
	v_lshlrev_b32_e32 v69, 16, v59
	v_pk_add_f32 v[62:63], v[62:63], v[66:67] neg_lo:[0,1] neg_hi:[0,1]
	s_waitcnt lgkmcnt(0)
	v_add_f32_e32 v59, v70, v71
	v_mul_f32_e32 v70, 0x4f800000, v59
	v_cmp_gt_f32_e32 vcc, s45, v59
	v_pk_fma_f32 v[62:63], v[50:51], v[62:63], v[66:67]
	v_pk_add_f32 v[66:67], v[68:69], v[66:67] neg_lo:[0,1] neg_hi:[0,1]
	v_cndmask_b32_e32 v59, v59, v70, vcc
	v_sqrt_f32_e32 v70, v59
	v_pk_fma_f32 v[62:63], v[52:53], v[66:67], v[62:63]
	v_add_u32_e32 v68, -1, v70
	v_fma_f32 v69, -v68, v70, v59
	v_cmp_ge_f32_e64 s[0:1], 0, v69
	v_add_u32_e32 v69, 1, v70
	s_nop 0
	v_cndmask_b32_e64 v68, v70, v68, s[0:1]
	v_fma_f32 v70, -v69, v70, v59
	v_cmp_lt_f32_e64 s[0:1], 0, v70
	s_nop 1
	v_cndmask_b32_e64 v68, v68, v69, s[0:1]
	v_mul_f32_e32 v69, 0x37800000, v68
	v_cndmask_b32_e32 v68, v68, v69, vcc
	v_cmp_class_f32_e32 vcc, v59, v207
	v_mad_i64_i32 v[66:67], s[0:1], s20, v214, v[46:47]
	s_nop 0
	v_cndmask_b32_e32 v59, v68, v59, vcc
	v_max_f32_e32 v59, 0x2b8cbccc, v59
	v_div_scale_f32 v68, s[0:1], v59, v59, v61
	v_rcp_f32_e32 v69, v68
	s_nop 0
	v_fma_f32 v70, -v68, v69, 1.0
	v_fmac_f32_e32 v69, v70, v69
	v_div_scale_f32 v70, vcc, v61, v59, v61
	v_mul_f32_e32 v71, v70, v69
	v_fma_f32 v72, -v68, v71, v70
	v_fmac_f32_e32 v71, v72, v69
	v_fma_f32 v68, -v68, v71, v70
	v_div_fmas_f32 v68, v68, v69, v71
	v_pk_add_f32 v[70:71], v[64:65], -1.0 op_sel_hi:[1,0]
	v_div_fixup_f32 v68, v68, v59, v61
	v_pk_fma_f32 v[70:71], v[48:49], v[70:71], 1.0 op_sel_hi:[1,1,0]
	v_pk_mul_f32 v[64:65], v[68:69], v[64:65] op_sel_hi:[0,1]
	v_pk_mul_f32 v[70:71], v[70:71], v[60:61] op_sel_hi:[1,0]
	v_mov_b32_e32 v61, v1
	v_add_f32_e32 v59, v70, v71
	v_mul_f32_e32 v59, v62, v59
	v_mul_f32_e32 v60, v56, v59
	v_cvt_pk_bf16_f32 v62, v62, v63
	v_cvt_pk_bf16_f32 v63, v68, 0
	v_mov_b32_dpp v61, v60 quad_perm:[1,0,3,2] row_mask:0xf bank_mask:0xf
	v_fmac_f32_e32 v61, v56, v59
	v_cvt_pk_bf16_f32 v64, v64, v65
	v_cvt_pk_bf16_f32 v65, v70, v71
	v_add_f32_dpp v59, v61, v61 quad_perm:[2,3,0,1] row_mask:0xf bank_mask:0xf bound_ctrl:1
	v_lshl_add_u64 v[68:69], v[66:67], 4, s[52:53]
	s_nop 0
	v_add_f32_dpp v59, v59, v59 row_half_mirror row_mask:0xf bank_mask:0xf bound_ctrl:1
	s_nop 1
	v_add_f32_dpp v59, v59, v59 row_mirror row_mask:0xf bank_mask:0xf bound_ctrl:1
	v_mov_b32_e32 v60, v59
	s_nop 1
	v_permlane32_swap_b32 v59, v60
	global_store_dwordx4 v[68:69], v[62:65], off
	v_add_f32_e32 v59, v59, v60
	v_mov_b32_e32 v60, v59
	s_nop 1
	v_permlane16_swap_b32_e32 v59, v60
	v_lshl_add_u64 v[64:65], v[66:67], 1, s[58:59]
	global_store_short_d16_hi v[64:65], v62, off
	s_and_saveexec_b64 s[0:1], s[42:43]
	s_cbranch_execz .LBB0_404
	s_waitcnt lgkmcnt(0)
	v_add_f32_e32 v59, v59, v60
	v_mad_i64_i32 v[60:61], s[20:21], s20, 24, v[114:115]
	global_store_dword v[60:61], v59, off
	s_branch .LBB0_404
